# v101 + nt on the norm+router phases' (5, 14) 16-byte loads: the split-K f32 slabs are read exactly once
# speedup vs baseline: 1.0078x; 1.0078x over previous
.LBB0_535:
	v_readlane_b32 s0, v250, 5
	s_mov_b32 s24, 0
	s_cmpk_gt_i32 s22, 0x41ff
	v_add_u32_e32 v16, s0, v78
	v_ashrrev_i32_e32 v17, 31, v16
	v_lshl_add_u64 v[66:67], v[16:17], 4, s[74:75]
	v_add_co_u32_e32 v0, vcc, 0xd20000, v66
	v_lshl_add_u32 v17, v16, 4, 0
	s_nop 0
	v_addc_co_u32_e32 v1, vcc, 0, v67, vcc
	v_add_co_u32_e32 v4, vcc, 0xd22000, v66
	v_readlane_b32 s1, v250, 6
	s_nop 0
	v_addc_co_u32_e32 v5, vcc, 0, v67, vcc
	v_add_co_u32_e32 v8, vcc, 0xd24000, v66
	global_load_dwordx4 v[0:3], v[0:1], off nt
	s_nop 0
	global_load_dwordx4 v[4:7], v[4:5], off nt
	v_addc_co_u32_e32 v9, vcc, 0, v67, vcc
	v_add_co_u32_e32 v12, vcc, 0xd26000, v66
	s_nop 1
	v_addc_co_u32_e32 v13, vcc, 0, v67, vcc
	v_add_co_u32_e32 v18, vcc, 0xd28000, v66
	global_load_dwordx4 v[8:11], v[8:9], off nt
	s_nop 0
	global_load_dwordx4 v[12:15], v[12:13], off nt
	v_addc_co_u32_e32 v19, vcc, 0, v67, vcc
	v_add_co_u32_e32 v22, vcc, 0xd2a000, v66
	s_nop 1
	v_addc_co_u32_e32 v23, vcc, 0, v67, vcc
	v_add_co_u32_e32 v26, vcc, 0xd2c000, v66
	global_load_dwordx4 v[18:21], v[18:19], off nt
	s_nop 0
	global_load_dwordx4 v[22:25], v[22:23], off nt
	v_addc_co_u32_e32 v27, vcc, 0, v67, vcc
	v_add_co_u32_e32 v30, vcc, 0xd2e000, v66
	s_nop 1
	v_addc_co_u32_e32 v31, vcc, 0, v67, vcc
	v_add_co_u32_e32 v34, vcc, 0xd30000, v66
	global_load_dwordx4 v[26:29], v[26:27], off nt
	s_nop 0
	global_load_dwordx4 v[30:33], v[30:31], off nt
	v_addc_co_u32_e32 v35, vcc, 0, v67, vcc
	v_add_co_u32_e32 v38, vcc, 0xd32000, v66
	s_nop 1
	v_addc_co_u32_e32 v39, vcc, 0, v67, vcc
	v_add_co_u32_e32 v42, vcc, 0xd34000, v66
	global_load_dwordx4 v[34:37], v[34:35], off nt
	s_nop 0
	global_load_dwordx4 v[38:41], v[38:39], off nt
	v_addc_co_u32_e32 v43, vcc, 0, v67, vcc
	v_add_co_u32_e32 v46, vcc, 0xd36000, v66
	s_nop 1
	v_addc_co_u32_e32 v47, vcc, 0, v67, vcc
	v_add_co_u32_e32 v50, vcc, 0xd38000, v66
	global_load_dwordx4 v[42:45], v[42:43], off nt
	s_nop 0
	global_load_dwordx4 v[46:49], v[46:47], off nt
	v_addc_co_u32_e32 v51, vcc, 0, v67, vcc
	v_add_co_u32_e32 v54, vcc, 0xd3a000, v66
	s_nop 1
	v_addc_co_u32_e32 v55, vcc, 0, v67, vcc
	v_add_co_u32_e32 v58, vcc, 0xd3c000, v66
	global_load_dwordx4 v[50:53], v[50:51], off nt
	s_nop 0
	global_load_dwordx4 v[54:57], v[54:55], off nt
	v_addc_co_u32_e32 v59, vcc, 0, v67, vcc
	v_add_co_u32_e32 v62, vcc, 0xd3e000, v66
	s_nop 1
	v_addc_co_u32_e32 v63, vcc, 0, v67, vcc
	v_add_co_u32_e32 v68, vcc, 0xd00000, v66
	global_load_dwordx4 v[58:61], v[58:59], off nt
	s_nop 0
	global_load_dwordx4 v[62:65], v[62:63], off nt
	v_addc_co_u32_e32 v69, vcc, 0, v67, vcc
	v_add_co_u32_e32 v70, vcc, 0xd02000, v66
	s_nop 1
	v_addc_co_u32_e32 v71, vcc, 0, v67, vcc
	global_load_dwordx4 v[66:69], v[68:69], off nt
	s_nop 0
	global_load_dwordx4 v[70:73], v[70:71], off nt
	s_waitcnt vmcnt(17)
	ds_write_b128 v17, v[0:3]
	s_waitcnt vmcnt(16)
	ds_write_b128 v17, v[4:7] offset:8192
	s_waitcnt vmcnt(15)
	ds_write_b128 v17, v[8:11] offset:16384
	s_waitcnt vmcnt(14)
	ds_write_b128 v17, v[12:15] offset:24576
	s_waitcnt vmcnt(13)
	ds_write_b128 v17, v[18:21] offset:32768
	s_waitcnt vmcnt(12)
	ds_write_b128 v17, v[22:25] offset:40960
	s_waitcnt vmcnt(11)
	ds_write_b128 v17, v[26:29] offset:49152
	s_waitcnt vmcnt(10)
	ds_write_b128 v17, v[30:33] offset:57344
	v_add_u32_e32 v0, 0x10000, v17
	s_waitcnt vmcnt(9)
	ds_write_b128 v0, v[34:37]
	v_add_u32_e32 v0, 0x12000, v17
	s_waitcnt vmcnt(8)
	ds_write_b128 v0, v[38:41]
	v_add_u32_e32 v0, 0x14000, v17
	s_waitcnt vmcnt(7)
	ds_write_b128 v0, v[42:45]
	v_add_u32_e32 v0, 0x16000, v17
	s_waitcnt vmcnt(6)
	ds_write_b128 v0, v[46:49]
	v_add_u32_e32 v0, 0x18000, v17
	s_waitcnt vmcnt(5)
	ds_write_b128 v0, v[50:53]
	v_add_u32_e32 v0, 0x1a000, v17
	s_waitcnt vmcnt(4)
	ds_write_b128 v0, v[54:57]
	v_add_u32_e32 v0, 0x1c000, v17
	s_waitcnt vmcnt(3)
	ds_write_b128 v0, v[58:61]
	v_add_u32_e32 v0, 0x1e000, v17
	s_waitcnt vmcnt(2)
	ds_write_b128 v0, v[62:65]
	v_add_u32_e32 v0, 0x20800, v17
	s_waitcnt vmcnt(1)
	ds_write_b128 v0, v[66:69]
	s_waitcnt vmcnt(0)
	ds_write_b128 v0, v[70:73] offset:8192
	s_waitcnt lgkmcnt(0)
	s_barrier
	s_cbranch_scc1 .LBB0_557
	v_and_b32_e32 v0, 32, v78
	v_lshlrev_b32_e32 v18, 2, v78
	v_cmp_eq_u32_e64 s[0:1], 0, v0
	v_and_b32_e32 v0, 16, v78
	s_add_u32 s26, s74, 0x8000
	v_ashrrev_i32_e32 v19, 31, v18
	v_cmp_eq_u32_e64 s[2:3], 0, v0
	v_and_b32_e32 v0, 8, v78
	v_readlane_b32 s76, v250, 7
	s_addc_u32 s27, s75, 0
	v_cmp_eq_u32_e64 s[4:5], 0, v0
	v_lshlrev_b64 v[0:1], 2, v[18:19]
	v_readlane_b32 s82, v250, 13
	v_readlane_b32 s83, v250, 14
	s_add_u32 s33, s74, 0x100000
	s_mov_b64 s[8:9], 0x1000
	v_lshl_add_u64 v[22:23], s[82:83], 0, v[0:1]
	s_addc_u32 s40, s75, 0
	v_lshl_add_u64 v[24:25], v[22:23], 0, s[8:9]
	s_mov_b64 s[8:9], 0x1400
	s_add_u32 s41, s74, 0x140000
	v_lshl_add_u64 v[26:27], v[22:23], 0, s[8:9]
	s_mov_b64 s[8:9], 0x1800
	s_addc_u32 s42, s75, 0
	v_lshl_add_u64 v[28:29], v[22:23], 0, s[8:9]
	s_mov_b64 s[8:9], 0x1c00
	s_add_u32 s28, s74, 0x3c400000
	v_lshl_add_u64 v[30:31], v[22:23], 0, s[8:9]
	s_addc_u32 s29, s75, 0
	v_lshl_add_u64 v[0:1], s[74:75], 0, v[0:1]
	s_mov_b64 s[8:9], 0x27a00000
	s_add_u32 s30, s74, 0x3c700000
	v_lshl_add_u64 v[32:33], v[0:1], 0, s[8:9]
	v_mbcnt_lo_u32_b32 v0, -1, 0
	v_lshl_add_u64 v[20:21], v[18:19], 1, s[96:97]
	v_cmp_eq_u32_e64 s[6:7], 0, v78
	s_addc_u32 s31, s75, 0
	s_add_i32 s34, s22, 0xffffc000
	s_movk_i32 s43, 0x1000
	s_mov_b32 s44, 0x400000
	s_mov_b32 s45, 0x401000
	s_mov_b32 s46, 0x800000
	s_mov_b32 s47, 0x801000
	s_mov_b32 s48, 0xc00000
	s_mov_b32 s49, 0xc01000
	s_mov_b64 s[36:37], 0x1000000
	v_mov_b32_e32 v35, 0
	v_mov_b32_e32 v17, 0x358637bd
	s_mov_b32 s54, 0xff61b1e6
	s_add_i32 s55, 0, 0x24900
	s_movk_i32 s56, 0x9f
	s_movk_i32 s57, 0x4200
	s_add_i32 s58, 0, 0x24800
	v_mov_b32_e32 v79, 1
	v_mbcnt_hi_u32_b32 v80, -1, v0
	v_mov_b32_e32 v81, 0xff61b1e6
	v_readlane_b32 s77, v250, 8
	v_readlane_b32 s78, v250, 9
	v_readlane_b32 s79, v250, 10
	v_readlane_b32 s80, v250, 11
	v_readlane_b32 s81, v250, 12
	v_readlane_b32 s84, v250, 15
	v_readlane_b32 s85, v250, 16
	v_readlane_b32 s86, v250, 17
	v_readlane_b32 s87, v250, 18
	v_readlane_b32 s88, v250, 19
	v_readlane_b32 s89, v250, 20
	v_readlane_b32 s90, v250, 21
	v_readlane_b32 s91, v250, 22
	s_branch .LBB0_538

.LBB0_542:
	v_add_co_u32_e32 v76, vcc, s43, v70
	global_load_dwordx4 v[12:15], v[70:71], off nt
	global_load_dwordx4 v[8:11], v[70:71], off offset:1024 nt
	global_load_dwordx4 v[4:7], v[70:71], off offset:2048 nt
	global_load_dwordx4 v[0:3], v[70:71], off offset:3072 nt
	v_addc_co_u32_e32 v77, vcc, 0, v71, vcc
	v_add_co_u32_e32 v114, vcc, s44, v70
	s_add_i32 s8, s8, 4
	s_nop 0
	v_addc_co_u32_e32 v115, vcc, 0, v71, vcc
	v_add_co_u32_e32 v178, vcc, s45, v70
	s_cmp_gt_u32 s8, 11
	s_nop 0
	v_addc_co_u32_e32 v179, vcc, 0, v71, vcc
	v_add_co_u32_e32 v118, vcc, s46, v70
	s_nop 1
	v_addc_co_u32_e32 v119, vcc, 0, v71, vcc
	v_add_co_u32_e32 v182, vcc, s47, v70
	s_nop 1
	v_addc_co_u32_e32 v183, vcc, 0, v71, vcc
	v_add_co_u32_e32 v122, vcc, s48, v70
	s_nop 1
	v_addc_co_u32_e32 v123, vcc, 0, v71, vcc
	v_add_co_u32_e32 v186, vcc, s49, v70
	s_nop 1
	v_addc_co_u32_e32 v187, vcc, 0, v71, vcc
	global_load_dwordx4 v[72:75], v[178:179], off offset:-4096 nt
	global_load_dwordx4 v[82:85], v[182:183], off offset:-4096 nt
	global_load_dwordx4 v[86:89], v[186:187], off offset:-4096 nt
	global_load_dwordx4 v[90:93], v[114:115], off offset:1024 nt
	global_load_dwordx4 v[94:97], v[118:119], off offset:1024 nt
	global_load_dwordx4 v[98:101], v[122:123], off offset:1024 nt
	global_load_dwordx4 v[102:105], v[114:115], off offset:2048 nt
	global_load_dwordx4 v[106:109], v[118:119], off offset:2048 nt
	global_load_dwordx4 v[110:113], v[122:123], off offset:2048 nt
	s_nop 0
	global_load_dwordx4 v[114:117], v[114:115], off offset:3072 nt
	s_nop 0
	global_load_dwordx4 v[118:121], v[118:119], off offset:3072 nt
	s_nop 0
	global_load_dwordx4 v[122:125], v[122:123], off offset:3072 nt
	s_nop 0
	global_load_dwordx4 v[126:129], v[76:77], off nt
	global_load_dwordx4 v[130:133], v[178:179], off nt
	global_load_dwordx4 v[134:137], v[182:183], off nt
	global_load_dwordx4 v[138:141], v[186:187], off nt
	global_load_dwordx4 v[142:145], v[76:77], off offset:1024 nt
	global_load_dwordx4 v[146:149], v[178:179], off offset:1024 nt
	global_load_dwordx4 v[150:153], v[182:183], off offset:1024 nt
	global_load_dwordx4 v[154:157], v[186:187], off offset:1024 nt
	global_load_dwordx4 v[158:161], v[76:77], off offset:2048 nt
	global_load_dwordx4 v[162:165], v[178:179], off offset:2048 nt
	global_load_dwordx4 v[166:169], v[182:183], off offset:2048 nt
	global_load_dwordx4 v[170:173], v[186:187], off offset:2048 nt
	global_load_dwordx4 v[174:177], v[76:77], off offset:3072 nt
	s_nop 0
	global_load_dwordx4 v[178:181], v[178:179], off offset:3072 nt
	s_nop 0
	global_load_dwordx4 v[182:185], v[182:183], off offset:3072 nt
	s_nop 0
	global_load_dwordx4 v[186:189], v[186:187], off offset:3072 nt
	v_lshl_add_u64 v[70:71], v[70:71], 0, s[36:37]
	s_waitcnt vmcnt(27)
	v_pk_add_f32 v[14:15], v[14:15], v[74:75]
	v_pk_add_f32 v[12:13], v[12:13], v[72:73]
	s_waitcnt vmcnt(25)
	v_pk_add_f32 v[72:73], v[84:85], v[88:89]
	v_pk_add_f32 v[74:75], v[82:83], v[86:87]
	s_waitcnt vmcnt(24)
	v_pk_add_f32 v[10:11], v[10:11], v[92:93]
	v_pk_add_f32 v[8:9], v[8:9], v[90:91]
	s_waitcnt vmcnt(22)
	v_pk_add_f32 v[76:77], v[96:97], v[100:101]
	v_pk_add_f32 v[82:83], v[94:95], v[98:99]
	s_waitcnt vmcnt(21)
	v_pk_add_f32 v[6:7], v[6:7], v[104:105]
	v_pk_add_f32 v[4:5], v[4:5], v[102:103]
	s_waitcnt vmcnt(19)
	v_pk_add_f32 v[84:85], v[108:109], v[112:113]
	v_pk_add_f32 v[86:87], v[106:107], v[110:111]
	s_waitcnt vmcnt(18)
	v_pk_add_f32 v[2:3], v[2:3], v[116:117]
	v_pk_add_f32 v[0:1], v[0:1], v[114:115]
	s_waitcnt vmcnt(16)
	v_pk_add_f32 v[88:89], v[120:121], v[124:125]
	v_pk_add_f32 v[90:91], v[118:119], v[122:123]
	s_waitcnt vmcnt(14)
	v_pk_add_f32 v[92:93], v[128:129], v[132:133]
	v_pk_add_f32 v[94:95], v[126:127], v[130:131]
	s_waitcnt vmcnt(12)
	v_pk_add_f32 v[96:97], v[136:137], v[140:141]
	v_pk_add_f32 v[98:99], v[134:135], v[138:139]
	s_waitcnt vmcnt(10)
	v_pk_add_f32 v[100:101], v[144:145], v[148:149]
	v_pk_add_f32 v[102:103], v[142:143], v[146:147]
	s_waitcnt vmcnt(8)
	v_pk_add_f32 v[104:105], v[152:153], v[156:157]
	v_pk_add_f32 v[106:107], v[150:151], v[154:155]
	s_waitcnt vmcnt(6)
	v_pk_add_f32 v[108:109], v[160:161], v[164:165]
	v_pk_add_f32 v[110:111], v[158:159], v[162:163]
	s_waitcnt vmcnt(4)
	v_pk_add_f32 v[112:113], v[168:169], v[172:173]
	v_pk_add_f32 v[114:115], v[166:167], v[170:171]
	s_waitcnt vmcnt(2)
	v_pk_add_f32 v[116:117], v[176:177], v[180:181]
	v_pk_add_f32 v[118:119], v[174:175], v[178:179]
	s_waitcnt vmcnt(0)
	v_pk_add_f32 v[120:121], v[184:185], v[188:189]
	v_pk_add_f32 v[122:123], v[182:183], v[186:187]
	v_pk_add_f32 v[14:15], v[14:15], v[72:73]
	v_pk_add_f32 v[12:13], v[12:13], v[74:75]
	v_pk_add_f32 v[10:11], v[10:11], v[76:77]
	v_pk_add_f32 v[8:9], v[8:9], v[82:83]
	v_pk_add_f32 v[6:7], v[6:7], v[84:85]
	v_pk_add_f32 v[4:5], v[4:5], v[86:87]
	v_pk_add_f32 v[2:3], v[2:3], v[88:89]
	v_pk_add_f32 v[0:1], v[0:1], v[90:91]
	v_pk_add_f32 v[72:73], v[92:93], v[96:97]
	v_pk_add_f32 v[74:75], v[94:95], v[98:99]
	v_pk_add_f32 v[76:77], v[100:101], v[104:105]
	v_pk_add_f32 v[82:83], v[102:103], v[106:107]
	v_pk_add_f32 v[84:85], v[108:109], v[112:113]
	v_pk_add_f32 v[86:87], v[110:111], v[114:115]
	v_pk_add_f32 v[88:89], v[116:117], v[120:121]
	v_pk_add_f32 v[90:91], v[118:119], v[122:123]
	v_pk_add_f32 v[46:47], v[46:47], v[14:15]
	v_pk_add_f32 v[36:37], v[36:37], v[12:13]
	v_pk_add_f32 v[54:55], v[54:55], v[10:11]
	v_pk_add_f32 v[42:43], v[42:43], v[8:9]
	v_pk_add_f32 v[60:61], v[60:61], v[6:7]
	v_pk_add_f32 v[48:49], v[48:49], v[4:5]
	v_pk_add_f32 v[64:65], v[64:65], v[2:3]
	v_pk_add_f32 v[58:59], v[58:59], v[0:1]
	v_pk_add_f32 v[66:67], v[66:67], v[72:73]
	v_pk_add_f32 v[62:63], v[62:63], v[74:75]
	v_pk_add_f32 v[50:51], v[50:51], v[76:77]
	v_pk_add_f32 v[38:39], v[38:39], v[82:83]
	v_pk_add_f32 v[56:57], v[56:57], v[84:85]
	v_pk_add_f32 v[44:45], v[44:45], v[86:87]
	v_pk_add_f32 v[52:53], v[52:53], v[88:89]
	v_pk_add_f32 v[40:41], v[40:41], v[90:91]
	s_cbranch_scc0 .LBB0_542
	v_cvt_pk_bf16_f32 v0, v36, v37
	v_cvt_pk_bf16_f32 v1, v46, v47
	global_store_dwordx2 v[68:69], v[0:1], off
	v_cvt_pk_bf16_f32 v0, v42, v43
	v_cvt_pk_bf16_f32 v1, v54, v55
	global_store_dwordx2 v[68:69], v[0:1], off offset:512
	v_cvt_pk_bf16_f32 v0, v48, v49
	v_cvt_pk_bf16_f32 v1, v60, v61
	global_store_dwordx2 v[68:69], v[0:1], off offset:1024
	v_cvt_pk_bf16_f32 v0, v58, v59
	v_cvt_pk_bf16_f32 v1, v64, v65
	global_store_dwordx2 v[68:69], v[0:1], off offset:1536
	v_cvt_pk_bf16_f32 v0, v62, v63
	v_cvt_pk_bf16_f32 v1, v66, v67
	global_store_dwordx2 v[68:69], v[0:1], off offset:2048
	v_cvt_pk_bf16_f32 v0, v38, v39
	v_cvt_pk_bf16_f32 v1, v50, v51
	global_store_dwordx2 v[68:69], v[0:1], off offset:2560
	v_cvt_pk_bf16_f32 v0, v44, v45
	v_cvt_pk_bf16_f32 v1, v56, v57
	global_store_dwordx2 v[68:69], v[0:1], off offset:3072
	v_cvt_pk_bf16_f32 v0, v40, v41
	v_cvt_pk_bf16_f32 v1, v52, v53
	global_store_dwordx2 v[68:69], v[0:1], off offset:3584
.LBB0_544:
	v_pk_mul_f32 v[10:11], v[36:37], v[36:37]
	v_pk_mul_f32 v[12:13], v[42:43], v[42:43]
	v_pk_mul_f32 v[4:5], v[46:47], v[46:47]
	v_pk_mul_f32 v[6:7], v[54:55], v[54:55]
	v_mov_b32_e32 v68, v10
	v_mov_b32_e32 v69, v12
	v_mov_b32_e32 v12, v11
	v_pk_mul_f32 v[0:1], v[60:61], v[60:61]
	v_pk_mul_f32 v[2:3], v[48:49], v[48:49]
	v_pk_add_f32 v[10:11], v[68:69], v[12:13]
	v_mov_b32_e32 v12, v4
	v_mov_b32_e32 v13, v6
	v_mov_b32_e32 v6, v5
	v_pk_add_f32 v[4:5], v[12:13], v[6:7]
	v_pk_mov_b32 v[6:7], v[2:3], v[0:1] op_sel:[1,0]
	v_mov_b32_e32 v3, v1
	v_pk_add_f32 v[0:1], v[6:7], v[2:3]
	v_pk_add_f32 v[4:5], v[10:11], v[4:5]
	v_pk_add_f32 v[0:1], v[0:1], v[0:1] op_sel_hi:[0,1]
	v_mul_f32_e32 v0, v58, v58
	v_pk_fma_f32 v[2:3], v[58:59], v[58:59], v[0:1] op_sel_hi:[1,1,0]
	v_mul_f32_e32 v0, v64, v64
	v_pk_add_f32 v[4:5], v[4:5], v[4:5] op_sel_hi:[0,1]
	v_pk_fma_f32 v[6:7], v[64:65], v[64:65], v[0:1] op_sel_hi:[1,1,0]
	v_mul_f32_e32 v2, v62, v62
	v_mul_f32_e32 v6, v63, v63
	v_mul_f32_e32 v0, v66, v66
	v_mul_f32_e32 v4, v67, v67
	v_pk_add_f32 v[2:3], v[2:3], v[6:7]
	v_pk_add_f32 v[0:1], v[0:1], v[4:5]
	global_load_dwordx4 v[4:7], v[22:23], off offset:1024 nt
	v_pk_add_f32 v[0:1], v[2:3], v[0:1]
	global_load_dwordx4 v[90:93], v[24:25], off nt
	global_load_dwordx4 v[94:97], v[26:27], off nt
	v_pk_add_f32 v[68:69], v[0:1], v[0:1] op_sel_hi:[0,1]
	global_load_dwordx4 v[0:3], v[22:23], off nt
	global_load_dwordx4 v[10:13], v[22:23], off offset:2048 nt
	global_load_dwordx4 v[86:89], v[22:23], off offset:3072 nt
	v_pk_mul_f32 v[8:9], v[50:51], v[50:51]
	v_pk_mul_f32 v[14:15], v[38:39], v[38:39]
	v_mul_f32_e32 v68, v53, v53
	v_pk_mov_b32 v[70:71], v[14:15], v[8:9] op_sel:[1,0]
	v_mov_b32_e32 v15, v9
	v_pk_add_f32 v[8:9], v[70:71], v[14:15]
	global_load_dwordx4 v[98:101], v[28:29], off nt
	global_load_dwordx4 v[102:105], v[30:31], off nt
	v_pk_add_f32 v[8:9], v[8:9], v[8:9] op_sel_hi:[0,1]
	v_mul_f32_e32 v8, v44, v44
	v_pk_fma_f32 v[14:15], v[44:45], v[44:45], v[8:9] op_sel_hi:[1,1,0]
	v_mul_f32_e32 v8, v56, v56
	v_pk_fma_f32 v[70:71], v[56:57], v[56:57], v[8:9] op_sel_hi:[1,1,0]
	v_mul_f32_e32 v14, v40, v40
	v_mul_f32_e32 v70, v41, v41
	v_mul_f32_e32 v8, v52, v52
	v_pk_add_f32 v[14:15], v[14:15], v[70:71]
	v_pk_add_f32 v[8:9], v[8:9], v[68:69]
	v_readlane_b32 s76, v250, 23
	v_pk_add_f32 v[8:9], v[14:15], v[8:9]
	v_readlane_b32 s84, v250, 31
	v_add_f32_e32 v8, v8, v9
	v_and_b32_e32 v9, 64, v80
	v_add_u32_e32 v14, 64, v9
	v_xor_b32_e32 v9, 1, v80
	v_cmp_lt_i32_e32 vcc, v9, v14
	v_readlane_b32 s85, v250, 32
	v_readlane_b32 s88, v250, 35
	v_cndmask_b32_e32 v9, v80, v9, vcc
	v_lshlrev_b32_e32 v9, 2, v9
	ds_bpermute_b32 v15, v9, v8
	v_readlane_b32 s89, v250, 36
	v_readlane_b32 s77, v250, 24
	v_readlane_b32 s78, v250, 25
	v_readlane_b32 s79, v250, 26
	s_waitcnt lgkmcnt(0)
	v_add_f32_e32 v8, v8, v15
	v_xor_b32_e32 v15, 2, v80
	v_cmp_lt_i32_e32 vcc, v15, v14
	v_readlane_b32 s80, v250, 27
	v_readlane_b32 s81, v250, 28
	v_cndmask_b32_e32 v15, v80, v15, vcc
	v_lshlrev_b32_e32 v34, 2, v15
	ds_bpermute_b32 v15, v34, v8
	v_readlane_b32 s82, v250, 29
	v_readlane_b32 s83, v250, 30
	v_readlane_b32 s86, v250, 33
	v_readlane_b32 s87, v250, 34
	s_waitcnt lgkmcnt(0)
	v_add_f32_e32 v8, v8, v15
	v_xor_b32_e32 v15, 4, v80
	v_cmp_lt_i32_e32 vcc, v15, v14
	v_readlane_b32 s90, v250, 37
	v_readlane_b32 s91, v250, 38
	v_cndmask_b32_e32 v15, v80, v15, vcc
	v_lshlrev_b32_e32 v82, 2, v15
	ds_bpermute_b32 v15, v82, v8
	s_waitcnt lgkmcnt(0)
	v_add_f32_e32 v8, v8, v15
	v_xor_b32_e32 v15, 8, v80
	v_cmp_lt_i32_e32 vcc, v15, v14
	s_waitcnt vmcnt(7)
	v_pk_mul_f32 v[72:73], v[42:43], v[4:5]
	v_cndmask_b32_e32 v15, v80, v15, vcc
	v_lshlrev_b32_e32 v83, 2, v15
	ds_bpermute_b32 v15, v83, v8
	v_pk_mul_f32 v[70:71], v[54:55], v[6:7]
	s_waitcnt vmcnt(4)
	v_pk_mul_f32 v[76:77], v[36:37], v[0:1]
	v_pk_mul_f32 v[74:75], v[46:47], v[2:3]
	v_pk_mul_f32 v[36:37], v[38:39], v[94:95]
	s_waitcnt lgkmcnt(0)
	v_add_f32_e32 v8, v8, v15
	v_xor_b32_e32 v15, 16, v80
	v_cmp_lt_i32_e32 vcc, v15, v14
	s_waitcnt vmcnt(3)
	v_pk_mul_f32 v[68:69], v[48:49], v[10:11]
	v_pk_mul_f32 v[60:61], v[60:61], v[12:13]
	v_cndmask_b32_e32 v15, v80, v15, vcc
	v_lshlrev_b32_e32 v84, 2, v15
	ds_bpermute_b32 v15, v84, v8
	s_waitcnt vmcnt(2)
	v_pk_mul_f32 v[54:55], v[58:59], v[86:87]
	v_pk_mul_f32 v[48:49], v[64:65], v[88:89]
	v_pk_mul_f32 v[46:47], v[62:63], v[90:91]
	v_pk_mul_f32 v[42:43], v[66:67], v[92:93]
	s_waitcnt lgkmcnt(0)
	v_add_f32_e32 v8, v8, v15
	v_xor_b32_e32 v15, 32, v80
	v_cmp_lt_i32_e32 vcc, v15, v14
	s_waitcnt vmcnt(1)
	v_pk_mul_f32 v[6:7], v[44:45], v[98:99]
	v_pk_mul_f32 v[4:5], v[56:57], v[100:101]
	v_cndmask_b32_e32 v14, v80, v15, vcc
	v_lshlrev_b32_e32 v85, 2, v14
	ds_bpermute_b32 v0, v85, v8
	v_pk_mul_f32 v[14:15], v[50:51], v[96:97]
	s_waitcnt vmcnt(0)
	v_pk_mul_f32 v[12:13], v[40:41], v[102:103]
	v_pk_mul_f32 v[10:11], v[52:53], v[104:105]
	s_waitcnt lgkmcnt(0)
	v_add_f32_e32 v0, v8, v0
	v_fmamk_f32 v0, v0, 0x3a000000, v17
	v_rsq_f32_e32 v8, v0
	v_lshl_add_u64 v[0:1], v[18:19], 1, s[38:39]
	v_mul_f32_e32 v2, v76, v8
	v_mul_f32_e32 v3, v77, v8
	v_cvt_pk_bf16_f32 v2, v2, v3
	v_mul_f32_e32 v3, v74, v8
	v_mul_f32_e32 v38, v75, v8
	v_cvt_pk_bf16_f32 v3, v3, v38
	global_store_dwordx2 v[0:1], v[2:3], off
	v_mul_f32_e32 v2, v72, v8
	v_mul_f32_e32 v3, v73, v8
	v_cvt_pk_bf16_f32 v2, v2, v3
	v_mul_f32_e32 v3, v70, v8
	v_mul_f32_e32 v38, v71, v8
	v_cvt_pk_bf16_f32 v3, v3, v38
	global_store_dwordx2 v[0:1], v[2:3], off offset:512
	v_mul_f32_e32 v2, v68, v8
	v_mul_f32_e32 v3, v69, v8
	v_cvt_pk_bf16_f32 v2, v2, v3
	v_mul_f32_e32 v3, v60, v8
	v_mul_f32_e32 v38, v61, v8
	v_cvt_pk_bf16_f32 v3, v3, v38
	global_store_dwordx2 v[0:1], v[2:3], off offset:1024
	v_mul_f32_e32 v2, v54, v8
	v_mul_f32_e32 v3, v55, v8
	v_cvt_pk_bf16_f32 v2, v2, v3
	v_mul_f32_e32 v3, v48, v8
	v_mul_f32_e32 v38, v49, v8
	v_cvt_pk_bf16_f32 v3, v3, v38
	global_store_dwordx2 v[0:1], v[2:3], off offset:1536
	v_mul_f32_e32 v2, v46, v8
	v_mul_f32_e32 v3, v47, v8
	v_cvt_pk_bf16_f32 v2, v2, v3
	v_mul_f32_e32 v3, v42, v8
	v_mul_f32_e32 v38, v43, v8
	v_cvt_pk_bf16_f32 v3, v3, v38
	global_store_dwordx2 v[0:1], v[2:3], off offset:2048
	v_mul_f32_e32 v2, v36, v8
	v_mul_f32_e32 v3, v37, v8
	v_cvt_pk_bf16_f32 v2, v2, v3
	v_mul_f32_e32 v3, v14, v8
	v_mul_f32_e32 v38, v15, v8
	v_cvt_pk_bf16_f32 v3, v3, v38
	global_store_dwordx2 v[0:1], v[2:3], off offset:2560
	v_mul_f32_e32 v2, v6, v8
	v_mul_f32_e32 v3, v7, v8
	v_cvt_pk_bf16_f32 v2, v2, v3
	v_mul_f32_e32 v3, v4, v8
	v_mul_f32_e32 v38, v5, v8
	v_cvt_pk_bf16_f32 v3, v3, v38
	global_store_dwordx2 v[0:1], v[2:3], off offset:3072
	v_mul_f32_e32 v2, v12, v8
	v_mul_f32_e32 v3, v13, v8
	v_cvt_pk_bf16_f32 v2, v2, v3
	v_mul_f32_e32 v3, v10, v8
	v_mul_f32_e32 v38, v11, v8
	v_cvt_pk_bf16_f32 v3, v3, v38
	global_store_dwordx2 v[0:1], v[2:3], off offset:3584
	v_mov_b32_e32 v0, v78
	s_nop 0
	v_lshl_add_u32 v0, v0, 3, 0
	v_add_u32_e32 v44, 0x20800, v0
	ds_read2st64_b64 v[0:3], v44 offset1:1
	ds_read2st64_b64 v[38:41], v44 offset0:2 offset1:3
	s_waitcnt lgkmcnt(1)
	v_fma_mix_f32 v45, v76, v0, 0 op_sel_hi:[0,1,0]
	v_fma_mix_f32 v0, v76, v0, 0 op_sel:[0,1,0] op_sel_hi:[0,1,0]
	v_fma_mix_f32 v50, v76, v1, 0 op_sel_hi:[0,1,0]
	v_fma_mix_f32 v1, v76, v1, 0 op_sel:[0,1,0] op_sel_hi:[0,1,0]
	v_fma_mix_f32 v45, v77, v2, v45 op_sel_hi:[0,1,0]
	v_fma_mix_f32 v0, v77, v2, v0 op_sel:[0,1,0] op_sel_hi:[0,1,0]
	v_fma_mix_f32 v2, v77, v3, v50 op_sel_hi:[0,1,0]
	v_fma_mix_f32 v1, v77, v3, v1 op_sel:[0,1,0] op_sel_hi:[0,1,0]
	s_waitcnt lgkmcnt(0)
	v_fma_mix_f32 v3, v74, v38, v45 op_sel_hi:[0,1,0]
	v_fma_mix_f32 v38, v74, v38, v0 op_sel:[0,1,0] op_sel_hi:[0,1,0]
	v_fma_mix_f32 v45, v74, v39, v2 op_sel_hi:[0,1,0]
	v_fma_mix_f32 v39, v74, v39, v1 op_sel:[0,1,0] op_sel_hi:[0,1,0]
	v_fma_mix_f32 v50, v75, v40, v3 op_sel_hi:[0,1,0]
	ds_read2st64_b64 v[0:3], v44 offset0:4 offset1:5
	v_fma_mix_f32 v51, v75, v40, v38 op_sel:[0,1,0] op_sel_hi:[0,1,0]
	v_fma_mix_f32 v45, v75, v41, v45 op_sel_hi:[0,1,0]
	v_fma_mix_f32 v52, v75, v41, v39 op_sel:[0,1,0] op_sel_hi:[0,1,0]
	ds_read2st64_b64 v[38:41], v44 offset0:6 offset1:7
	s_waitcnt lgkmcnt(1)
	v_fma_mix_f32 v50, v72, v0, v50 op_sel_hi:[0,1,0]
	v_fma_mix_f32 v0, v72, v0, v51 op_sel:[0,1,0] op_sel_hi:[0,1,0]
	v_fma_mix_f32 v45, v72, v1, v45 op_sel_hi:[0,1,0]
	v_fma_mix_f32 v1, v72, v1, v52 op_sel:[0,1,0] op_sel_hi:[0,1,0]
	v_fma_mix_f32 v50, v73, v2, v50 op_sel_hi:[0,1,0]
	v_fma_mix_f32 v0, v73, v2, v0 op_sel:[0,1,0] op_sel_hi:[0,1,0]
	v_fma_mix_f32 v2, v73, v3, v45 op_sel_hi:[0,1,0]
	v_fma_mix_f32 v1, v73, v3, v1 op_sel:[0,1,0] op_sel_hi:[0,1,0]
	s_waitcnt lgkmcnt(0)
	v_fma_mix_f32 v3, v70, v38, v50 op_sel_hi:[0,1,0]
	v_fma_mix_f32 v38, v70, v38, v0 op_sel:[0,1,0] op_sel_hi:[0,1,0]
	v_fma_mix_f32 v45, v70, v39, v2 op_sel_hi:[0,1,0]
	v_fma_mix_f32 v39, v70, v39, v1 op_sel:[0,1,0] op_sel_hi:[0,1,0]
	v_fma_mix_f32 v50, v71, v40, v3 op_sel_hi:[0,1,0]
	ds_read2st64_b64 v[0:3], v44 offset0:8 offset1:9
	v_fma_mix_f32 v51, v71, v40, v38 op_sel:[0,1,0] op_sel_hi:[0,1,0]
	v_fma_mix_f32 v45, v71, v41, v45 op_sel_hi:[0,1,0]
	v_fma_mix_f32 v52, v71, v41, v39 op_sel:[0,1,0] op_sel_hi:[0,1,0]
	ds_read2st64_b64 v[38:41], v44 offset0:10 offset1:11
	s_waitcnt lgkmcnt(1)
	v_fma_mix_f32 v50, v68, v0, v50 op_sel_hi:[0,1,0]
	v_fma_mix_f32 v0, v68, v0, v51 op_sel:[0,1,0] op_sel_hi:[0,1,0]
	v_fma_mix_f32 v45, v68, v1, v45 op_sel_hi:[0,1,0]
	v_fma_mix_f32 v1, v68, v1, v52 op_sel:[0,1,0] op_sel_hi:[0,1,0]
	v_fma_mix_f32 v50, v69, v2, v50 op_sel_hi:[0,1,0]
	v_fma_mix_f32 v0, v69, v2, v0 op_sel:[0,1,0] op_sel_hi:[0,1,0]
	v_fma_mix_f32 v2, v69, v3, v45 op_sel_hi:[0,1,0]
	v_fma_mix_f32 v1, v69, v3, v1 op_sel:[0,1,0] op_sel_hi:[0,1,0]
	s_waitcnt lgkmcnt(0)
	v_fma_mix_f32 v3, v60, v38, v50 op_sel_hi:[0,1,0]
	v_fma_mix_f32 v38, v60, v38, v0 op_sel:[0,1,0] op_sel_hi:[0,1,0]
	v_fma_mix_f32 v45, v60, v39, v2 op_sel_hi:[0,1,0]
	v_fma_mix_f32 v39, v60, v39, v1 op_sel:[0,1,0] op_sel_hi:[0,1,0]
	v_fma_mix_f32 v50, v61, v40, v3 op_sel_hi:[0,1,0]
	ds_read2st64_b64 v[0:3], v44 offset0:12 offset1:13
	v_fma_mix_f32 v51, v61, v40, v38 op_sel:[0,1,0] op_sel_hi:[0,1,0]
	v_fma_mix_f32 v45, v61, v41, v45 op_sel_hi:[0,1,0]
	v_fma_mix_f32 v52, v61, v41, v39 op_sel:[0,1,0] op_sel_hi:[0,1,0]
	ds_read2st64_b64 v[38:41], v44 offset0:14 offset1:15
	s_waitcnt lgkmcnt(1)
	v_fma_mix_f32 v50, v54, v0, v50 op_sel_hi:[0,1,0]
	v_fma_mix_f32 v0, v54, v0, v51 op_sel:[0,1,0] op_sel_hi:[0,1,0]
	v_fma_mix_f32 v45, v54, v1, v45 op_sel_hi:[0,1,0]
	v_fma_mix_f32 v1, v54, v1, v52 op_sel:[0,1,0] op_sel_hi:[0,1,0]
	v_fma_mix_f32 v50, v55, v2, v50 op_sel_hi:[0,1,0]
	v_fma_mix_f32 v0, v55, v2, v0 op_sel:[0,1,0] op_sel_hi:[0,1,0]
	v_fma_mix_f32 v2, v55, v3, v45 op_sel_hi:[0,1,0]
	v_fma_mix_f32 v1, v55, v3, v1 op_sel:[0,1,0] op_sel_hi:[0,1,0]
	s_waitcnt lgkmcnt(0)
	v_fma_mix_f32 v3, v48, v38, v50 op_sel_hi:[0,1,0]
	v_fma_mix_f32 v38, v48, v38, v0 op_sel:[0,1,0] op_sel_hi:[0,1,0]
	v_fma_mix_f32 v45, v48, v39, v2 op_sel_hi:[0,1,0]
	v_fma_mix_f32 v39, v48, v39, v1 op_sel:[0,1,0] op_sel_hi:[0,1,0]
	v_fma_mix_f32 v50, v49, v40, v3 op_sel_hi:[0,1,0]
	ds_read2st64_b64 v[0:3], v44 offset0:16 offset1:17
	v_fma_mix_f32 v51, v49, v40, v38 op_sel:[0,1,0] op_sel_hi:[0,1,0]
	v_fma_mix_f32 v45, v49, v41, v45 op_sel_hi:[0,1,0]
	v_fma_mix_f32 v52, v49, v41, v39 op_sel:[0,1,0] op_sel_hi:[0,1,0]
	ds_read2st64_b64 v[38:41], v44 offset0:18 offset1:19
	s_waitcnt lgkmcnt(1)
	v_fma_mix_f32 v50, v46, v0, v50 op_sel_hi:[0,1,0]
	v_fma_mix_f32 v0, v46, v0, v51 op_sel:[0,1,0] op_sel_hi:[0,1,0]
	v_fma_mix_f32 v45, v46, v1, v45 op_sel_hi:[0,1,0]
	v_fma_mix_f32 v1, v46, v1, v52 op_sel:[0,1,0] op_sel_hi:[0,1,0]
	v_fma_mix_f32 v50, v47, v2, v50 op_sel_hi:[0,1,0]
	v_fma_mix_f32 v0, v47, v2, v0 op_sel:[0,1,0] op_sel_hi:[0,1,0]
	v_fma_mix_f32 v2, v47, v3, v45 op_sel_hi:[0,1,0]
	v_fma_mix_f32 v1, v47, v3, v1 op_sel:[0,1,0] op_sel_hi:[0,1,0]
	s_waitcnt lgkmcnt(0)
	v_fma_mix_f32 v3, v42, v38, v50 op_sel_hi:[0,1,0]
	v_fma_mix_f32 v38, v42, v38, v0 op_sel:[0,1,0] op_sel_hi:[0,1,0]
	v_fma_mix_f32 v45, v42, v39, v2 op_sel_hi:[0,1,0]
	v_fma_mix_f32 v39, v42, v39, v1 op_sel:[0,1,0] op_sel_hi:[0,1,0]
	v_fma_mix_f32 v50, v43, v40, v3 op_sel_hi:[0,1,0]
	ds_read2st64_b64 v[0:3], v44 offset0:20 offset1:21
	v_fma_mix_f32 v51, v43, v40, v38 op_sel:[0,1,0] op_sel_hi:[0,1,0]
	v_fma_mix_f32 v45, v43, v41, v45 op_sel_hi:[0,1,0]
	v_fma_mix_f32 v52, v43, v41, v39 op_sel:[0,1,0] op_sel_hi:[0,1,0]
	ds_read2st64_b64 v[38:41], v44 offset0:22 offset1:23
	s_waitcnt lgkmcnt(1)
	v_fma_mix_f32 v50, v36, v0, v50 op_sel_hi:[0,1,0]
	v_fma_mix_f32 v0, v36, v0, v51 op_sel:[0,1,0] op_sel_hi:[0,1,0]
	v_fma_mix_f32 v45, v36, v1, v45 op_sel_hi:[0,1,0]
	v_fma_mix_f32 v1, v36, v1, v52 op_sel:[0,1,0] op_sel_hi:[0,1,0]
	v_fma_mix_f32 v50, v37, v2, v50 op_sel_hi:[0,1,0]
	v_fma_mix_f32 v0, v37, v2, v0 op_sel:[0,1,0] op_sel_hi:[0,1,0]
	v_fma_mix_f32 v2, v37, v3, v45 op_sel_hi:[0,1,0]
	v_fma_mix_f32 v1, v37, v3, v1 op_sel:[0,1,0] op_sel_hi:[0,1,0]
	s_waitcnt lgkmcnt(0)
	v_fma_mix_f32 v3, v14, v38, v50 op_sel_hi:[0,1,0]
	v_fma_mix_f32 v38, v14, v38, v0 op_sel:[0,1,0] op_sel_hi:[0,1,0]
	v_fma_mix_f32 v45, v14, v39, v2 op_sel_hi:[0,1,0]
	v_fma_mix_f32 v39, v14, v39, v1 op_sel:[0,1,0] op_sel_hi:[0,1,0]
	v_fma_mix_f32 v50, v15, v40, v3 op_sel_hi:[0,1,0]
	ds_read2st64_b64 v[0:3], v44 offset0:24 offset1:25
	v_fma_mix_f32 v51, v15, v40, v38 op_sel:[0,1,0] op_sel_hi:[0,1,0]
	v_fma_mix_f32 v45, v15, v41, v45 op_sel_hi:[0,1,0]
	v_fma_mix_f32 v52, v15, v41, v39 op_sel:[0,1,0] op_sel_hi:[0,1,0]
	ds_read2st64_b64 v[38:41], v44 offset0:26 offset1:27
	s_waitcnt lgkmcnt(1)
	v_fma_mix_f32 v50, v6, v0, v50 op_sel_hi:[0,1,0]
	v_fma_mix_f32 v0, v6, v0, v51 op_sel:[0,1,0] op_sel_hi:[0,1,0]
	v_fma_mix_f32 v45, v6, v1, v45 op_sel_hi:[0,1,0]
	v_fma_mix_f32 v1, v6, v1, v52 op_sel:[0,1,0] op_sel_hi:[0,1,0]
	v_fma_mix_f32 v50, v7, v2, v50 op_sel_hi:[0,1,0]
	v_fma_mix_f32 v51, v7, v2, v0 op_sel:[0,1,0] op_sel_hi:[0,1,0]
	v_fma_mix_f32 v45, v7, v3, v45 op_sel_hi:[0,1,0]
	v_fma_mix_f32 v52, v7, v3, v1 op_sel:[0,1,0] op_sel_hi:[0,1,0]
	global_load_dwordx4 v[0:3], v35, s[84:85] nt
	s_waitcnt lgkmcnt(0)
	v_fma_mix_f32 v50, v4, v38, v50 op_sel_hi:[0,1,0]
	v_fma_mix_f32 v38, v4, v38, v51 op_sel:[0,1,0] op_sel_hi:[0,1,0]
	v_fma_mix_f32 v45, v4, v39, v45 op_sel_hi:[0,1,0]
	v_fma_mix_f32 v39, v4, v39, v52 op_sel:[0,1,0] op_sel_hi:[0,1,0]
	v_fma_mix_f32 v56, v5, v40, v50 op_sel_hi:[0,1,0]
	ds_read2st64_b64 v[50:53], v44 offset0:28 offset1:29
	v_fma_mix_f32 v57, v5, v40, v38 op_sel:[0,1,0] op_sel_hi:[0,1,0]
	v_fma_mix_f32 v45, v5, v41, v45 op_sel_hi:[0,1,0]
	v_fma_mix_f32 v58, v5, v41, v39 op_sel:[0,1,0] op_sel_hi:[0,1,0]
	ds_read2st64_b64 v[38:41], v44 offset0:30 offset1:31
	s_waitcnt lgkmcnt(1)
	v_fma_mix_f32 v44, v12, v50, v56 op_sel_hi:[0,1,0]
	v_fma_mix_f32 v50, v12, v50, v57 op_sel:[0,1,0] op_sel_hi:[0,1,0]
	v_fma_mix_f32 v45, v12, v51, v45 op_sel_hi:[0,1,0]
	v_fma_mix_f32 v56, v13, v52, v44 op_sel_hi:[0,1,0]
	v_fma_mix_f32 v50, v13, v52, v50 op_sel:[0,1,0] op_sel_hi:[0,1,0]
	v_fma_mix_f32 v52, v13, v53, v45 op_sel_hi:[0,1,0]
	s_waitcnt lgkmcnt(0)
	v_cvt_f32_f16_sdwa v45, v40 dst_sel:DWORD dst_unused:UNUSED_PAD src0_sel:WORD_1
	v_cvt_f32_f16_sdwa v44, v38 dst_sel:DWORD dst_unused:UNUSED_PAD src0_sel:WORD_1
	v_fma_mix_f32 v51, v12, v51, v58 op_sel:[0,1,0] op_sel_hi:[0,1,0]
	v_fma_mix_f32 v38, v10, v38, v56 op_sel_hi:[0,1,0]
	v_fma_mix_f32 v53, v13, v53, v51 op_sel:[0,1,0] op_sel_hi:[0,1,0]
	v_pk_mul_f32 v[44:45], v[10:11], v[44:45]
	v_fma_mix_f32 v56, v11, v40, v38 op_sel_hi:[0,1,0]
	v_add_f32_e32 v38, v44, v50
	v_cvt_f32_f16_e32 v51, v41
	v_cvt_f32_f16_e32 v50, v39
	v_cvt_f32_f16_sdwa v41, v41 dst_sel:DWORD dst_unused:UNUSED_PAD src0_sel:WORD_1
	v_cvt_f32_f16_sdwa v40, v39 dst_sel:DWORD dst_unused:UNUSED_PAD src0_sel:WORD_1
	v_add_f32_e32 v44, v45, v38
	v_pk_mul_f32 v[38:39], v[10:11], v[50:51]
	s_nop 0
	v_add_f32_e32 v38, v38, v52
	v_add_f32_e32 v45, v39, v38
	v_pk_mul_f32 v[38:39], v[10:11], v[40:41]
	v_cndmask_b32_e64 v41, v44, v56, s[0:1]
	v_add_f32_e32 v38, v38, v53
	v_add_f32_e32 v38, v39, v38
	v_cndmask_b32_e64 v39, v56, v44, s[0:1]
	v_cndmask_b32_e64 v40, v45, v38, s[0:1]
	ds_bpermute_b32 v39, v85, v39
	ds_bpermute_b32 v40, v85, v40
	v_cndmask_b32_e64 v38, v38, v45, s[0:1]
	s_waitcnt lgkmcnt(1)
	v_add_f32_e32 v39, v41, v39
	s_waitcnt lgkmcnt(0)
	v_add_f32_e32 v38, v38, v40
	v_cndmask_b32_e64 v40, v39, v38, s[2:3]
	ds_bpermute_b32 v40, v84, v40
	v_cndmask_b32_e64 v38, v38, v39, s[2:3]
	s_waitcnt lgkmcnt(0)
	v_add_f32_e32 v38, v38, v40
	ds_bpermute_b32 v39, v83, v38
	s_waitcnt lgkmcnt(0)
	v_add_f32_e32 v38, v38, v39
	ds_bpermute_b32 v39, v82, v38
	s_waitcnt lgkmcnt(0)
	v_add_f32_e32 v38, v38, v39
	ds_bpermute_b32 v39, v34, v38
	s_waitcnt lgkmcnt(0)
	v_add_f32_e32 v38, v38, v39
	ds_bpermute_b32 v39, v9, v38
	s_waitcnt lgkmcnt(0)
	v_add_f32_e32 v38, v38, v39
	s_nop 0
	v_readlane_b32 s8, v38, 0
	v_readlane_b32 s9, v38, 32
	v_readlane_b32 s10, v38, 16
	v_readlane_b32 s11, v38, 48
	s_waitcnt vmcnt(0)
	v_pk_fma_f32 v[38:39], v[8:9], s[8:9], v[0:1] op_sel_hi:[0,1,1]
	v_cmp_gt_f32_e32 vcc, v39, v38
	v_fma_f32 v0, s10, v8, v2
	v_fmac_f32_e32 v3, s11, v8
	v_cndmask_b32_e32 v1, v38, v39, vcc
	v_cmp_gt_f32_e64 s[8:9], v0, v1
	s_nop 1
	v_cndmask_b32_e64 v40, v1, v0, s[8:9]
	v_cndmask_b32_e64 v1, 0, 1, vcc
	v_cndmask_b32_e64 v1, v1, 2, s[8:9]
	v_cmp_gt_f32_e32 vcc, v3, v40
	s_nop 1
	v_cndmask_b32_e64 v1, v1, 3, vcc
	v_lshl_add_u32 v2, v1, 6, v78
	s_nop 0
	v_lshl_add_u32 v2, v2, 4, 0
	ds_read_b128 v[50:53], v2
	ds_read_b128 v[56:59], v2 offset:4096
	s_waitcnt lgkmcnt(1)
	v_fma_mix_f32 v41, v76, v50, 0 op_sel_hi:[0,1,0]
	v_fma_mix_f32 v44, v76, v50, 0 op_sel:[0,1,0] op_sel_hi:[0,1,0]
	v_fma_mix_f32 v45, v76, v51, 0 op_sel_hi:[0,1,0]
	v_fma_mix_f32 v50, v76, v51, 0 op_sel:[0,1,0] op_sel_hi:[0,1,0]
	v_fma_mix_f32 v51, v76, v52, 0 op_sel_hi:[0,1,0]
	v_fma_mix_f32 v62, v76, v52, 0 op_sel:[0,1,0] op_sel_hi:[0,1,0]
	v_fma_mix_f32 v63, v76, v53, 0 op_sel_hi:[0,1,0]
	v_fma_mix_f32 v64, v76, v53, 0 op_sel:[0,1,0] op_sel_hi:[0,1,0]
	s_waitcnt lgkmcnt(0)
	v_fma_mix_f32 v65, v77, v57, v50 op_sel:[0,1,0] op_sel_hi:[0,1,0]
	v_fma_mix_f32 v66, v77, v58, v51 op_sel_hi:[0,1,0]
	ds_read_b128 v[50:53], v2 offset:8192
	v_fma_mix_f32 v41, v77, v56, v41 op_sel_hi:[0,1,0]
	v_fma_mix_f32 v44, v77, v56, v44 op_sel:[0,1,0] op_sel_hi:[0,1,0]
	v_fma_mix_f32 v45, v77, v57, v45 op_sel_hi:[0,1,0]
	v_fma_mix_f32 v62, v77, v58, v62 op_sel:[0,1,0] op_sel_hi:[0,1,0]
	v_fma_mix_f32 v63, v77, v59, v63 op_sel_hi:[0,1,0]
	v_fma_mix_f32 v64, v77, v59, v64 op_sel:[0,1,0] op_sel_hi:[0,1,0]
	ds_read_b128 v[56:59], v2 offset:12288
	s_waitcnt lgkmcnt(1)
	v_fma_mix_f32 v41, v74, v50, v41 op_sel_hi:[0,1,0]
	v_fma_mix_f32 v44, v74, v50, v44 op_sel:[0,1,0] op_sel_hi:[0,1,0]
	v_fma_mix_f32 v45, v74, v51, v45 op_sel_hi:[0,1,0]
	v_fma_mix_f32 v50, v74, v51, v65 op_sel:[0,1,0] op_sel_hi:[0,1,0]
	v_fma_mix_f32 v51, v74, v52, v66 op_sel_hi:[0,1,0]
	v_fma_mix_f32 v62, v74, v52, v62 op_sel:[0,1,0] op_sel_hi:[0,1,0]
	v_fma_mix_f32 v63, v74, v53, v63 op_sel_hi:[0,1,0]
	v_fma_mix_f32 v64, v74, v53, v64 op_sel:[0,1,0] op_sel_hi:[0,1,0]
	s_waitcnt lgkmcnt(0)
	v_fma_mix_f32 v65, v75, v57, v50 op_sel:[0,1,0] op_sel_hi:[0,1,0]
	v_fma_mix_f32 v66, v75, v58, v51 op_sel_hi:[0,1,0]
	ds_read_b128 v[50:53], v2 offset:16384
	v_fma_mix_f32 v41, v75, v56, v41 op_sel_hi:[0,1,0]
	v_fma_mix_f32 v44, v75, v56, v44 op_sel:[0,1,0] op_sel_hi:[0,1,0]
	v_fma_mix_f32 v45, v75, v57, v45 op_sel_hi:[0,1,0]
	v_fma_mix_f32 v62, v75, v58, v62 op_sel:[0,1,0] op_sel_hi:[0,1,0]
	v_fma_mix_f32 v63, v75, v59, v63 op_sel_hi:[0,1,0]
	v_fma_mix_f32 v64, v75, v59, v64 op_sel:[0,1,0] op_sel_hi:[0,1,0]
	ds_read_b128 v[56:59], v2 offset:20480
	s_waitcnt lgkmcnt(1)
	v_fma_mix_f32 v41, v72, v50, v41 op_sel_hi:[0,1,0]
	v_fma_mix_f32 v44, v72, v50, v44 op_sel:[0,1,0] op_sel_hi:[0,1,0]
	v_fma_mix_f32 v45, v72, v51, v45 op_sel_hi:[0,1,0]
	v_fma_mix_f32 v50, v72, v51, v65 op_sel:[0,1,0] op_sel_hi:[0,1,0]
	v_fma_mix_f32 v51, v72, v52, v66 op_sel_hi:[0,1,0]
	v_fma_mix_f32 v62, v72, v52, v62 op_sel:[0,1,0] op_sel_hi:[0,1,0]
	v_fma_mix_f32 v63, v72, v53, v63 op_sel_hi:[0,1,0]
	v_fma_mix_f32 v64, v72, v53, v64 op_sel:[0,1,0] op_sel_hi:[0,1,0]
	s_waitcnt lgkmcnt(0)
	v_fma_mix_f32 v65, v73, v57, v50 op_sel:[0,1,0] op_sel_hi:[0,1,0]
	v_fma_mix_f32 v66, v73, v58, v51 op_sel_hi:[0,1,0]
	ds_read_b128 v[50:53], v2 offset:24576
	v_fma_mix_f32 v41, v73, v56, v41 op_sel_hi:[0,1,0]
	v_fma_mix_f32 v44, v73, v56, v44 op_sel:[0,1,0] op_sel_hi:[0,1,0]
	v_fma_mix_f32 v45, v73, v57, v45 op_sel_hi:[0,1,0]
	v_fma_mix_f32 v62, v73, v58, v62 op_sel:[0,1,0] op_sel_hi:[0,1,0]
	v_fma_mix_f32 v63, v73, v59, v63 op_sel_hi:[0,1,0]
	v_fma_mix_f32 v64, v73, v59, v64 op_sel:[0,1,0] op_sel_hi:[0,1,0]
	ds_read_b128 v[56:59], v2 offset:28672
	s_waitcnt lgkmcnt(1)
	v_fma_mix_f32 v41, v70, v50, v41 op_sel_hi:[0,1,0]
	v_fma_mix_f32 v44, v70, v50, v44 op_sel:[0,1,0] op_sel_hi:[0,1,0]
	v_fma_mix_f32 v45, v70, v51, v45 op_sel_hi:[0,1,0]
	v_fma_mix_f32 v50, v70, v51, v65 op_sel:[0,1,0] op_sel_hi:[0,1,0]
	v_fma_mix_f32 v51, v70, v52, v66 op_sel_hi:[0,1,0]
	v_fma_mix_f32 v62, v70, v52, v62 op_sel:[0,1,0] op_sel_hi:[0,1,0]
	v_fma_mix_f32 v63, v70, v53, v63 op_sel_hi:[0,1,0]
	v_fma_mix_f32 v64, v70, v53, v64 op_sel:[0,1,0] op_sel_hi:[0,1,0]
	s_waitcnt lgkmcnt(0)
	v_fma_mix_f32 v65, v71, v57, v50 op_sel:[0,1,0] op_sel_hi:[0,1,0]
	v_fma_mix_f32 v66, v71, v58, v51 op_sel_hi:[0,1,0]
	ds_read_b128 v[50:53], v2 offset:32768
	v_fma_mix_f32 v41, v71, v56, v41 op_sel_hi:[0,1,0]
	v_fma_mix_f32 v44, v71, v56, v44 op_sel:[0,1,0] op_sel_hi:[0,1,0]
	v_fma_mix_f32 v45, v71, v57, v45 op_sel_hi:[0,1,0]
	v_fma_mix_f32 v62, v71, v58, v62 op_sel:[0,1,0] op_sel_hi:[0,1,0]
	v_fma_mix_f32 v63, v71, v59, v63 op_sel_hi:[0,1,0]
	v_fma_mix_f32 v64, v71, v59, v64 op_sel:[0,1,0] op_sel_hi:[0,1,0]
	ds_read_b128 v[56:59], v2 offset:36864
	s_waitcnt lgkmcnt(1)
	v_fma_mix_f32 v41, v68, v50, v41 op_sel_hi:[0,1,0]
	v_fma_mix_f32 v44, v68, v50, v44 op_sel:[0,1,0] op_sel_hi:[0,1,0]
	v_fma_mix_f32 v45, v68, v51, v45 op_sel_hi:[0,1,0]
	v_fma_mix_f32 v50, v68, v51, v65 op_sel:[0,1,0] op_sel_hi:[0,1,0]
	v_fma_mix_f32 v51, v68, v52, v66 op_sel_hi:[0,1,0]
	v_fma_mix_f32 v62, v68, v52, v62 op_sel:[0,1,0] op_sel_hi:[0,1,0]
	v_fma_mix_f32 v63, v68, v53, v63 op_sel_hi:[0,1,0]
	v_fma_mix_f32 v64, v68, v53, v64 op_sel:[0,1,0] op_sel_hi:[0,1,0]
	s_waitcnt lgkmcnt(0)
	v_fma_mix_f32 v65, v69, v57, v50 op_sel:[0,1,0] op_sel_hi:[0,1,0]
	v_fma_mix_f32 v66, v69, v58, v51 op_sel_hi:[0,1,0]
	ds_read_b128 v[50:53], v2 offset:40960
	v_fma_mix_f32 v41, v69, v56, v41 op_sel_hi:[0,1,0]
	v_fma_mix_f32 v44, v69, v56, v44 op_sel:[0,1,0] op_sel_hi:[0,1,0]
	v_fma_mix_f32 v45, v69, v57, v45 op_sel_hi:[0,1,0]
	v_fma_mix_f32 v62, v69, v58, v62 op_sel:[0,1,0] op_sel_hi:[0,1,0]
	v_fma_mix_f32 v63, v69, v59, v63 op_sel_hi:[0,1,0]
	v_fma_mix_f32 v64, v69, v59, v64 op_sel:[0,1,0] op_sel_hi:[0,1,0]
	ds_read_b128 v[56:59], v2 offset:45056
	s_waitcnt lgkmcnt(1)
	v_fma_mix_f32 v41, v60, v50, v41 op_sel_hi:[0,1,0]
	v_fma_mix_f32 v44, v60, v50, v44 op_sel:[0,1,0] op_sel_hi:[0,1,0]
	v_fma_mix_f32 v45, v60, v51, v45 op_sel_hi:[0,1,0]
	v_fma_mix_f32 v50, v60, v51, v65 op_sel:[0,1,0] op_sel_hi:[0,1,0]
	v_fma_mix_f32 v51, v60, v52, v66 op_sel_hi:[0,1,0]
	v_fma_mix_f32 v62, v60, v52, v62 op_sel:[0,1,0] op_sel_hi:[0,1,0]
	v_fma_mix_f32 v63, v60, v53, v63 op_sel_hi:[0,1,0]
	v_fma_mix_f32 v60, v60, v53, v64 op_sel:[0,1,0] op_sel_hi:[0,1,0]
	s_waitcnt lgkmcnt(0)
	v_fma_mix_f32 v64, v61, v57, v50 op_sel:[0,1,0] op_sel_hi:[0,1,0]
	v_fma_mix_f32 v65, v61, v58, v51 op_sel_hi:[0,1,0]
	ds_read_b128 v[50:53], v2 offset:49152
	v_fma_mix_f32 v41, v61, v56, v41 op_sel_hi:[0,1,0]
	v_fma_mix_f32 v44, v61, v56, v44 op_sel:[0,1,0] op_sel_hi:[0,1,0]
	v_fma_mix_f32 v45, v61, v57, v45 op_sel_hi:[0,1,0]
	v_fma_mix_f32 v62, v61, v58, v62 op_sel:[0,1,0] op_sel_hi:[0,1,0]
	v_fma_mix_f32 v63, v61, v59, v63 op_sel_hi:[0,1,0]
	v_fma_mix_f32 v60, v61, v59, v60 op_sel:[0,1,0] op_sel_hi:[0,1,0]
	ds_read_b128 v[56:59], v2 offset:53248
	s_waitcnt lgkmcnt(1)
	v_fma_mix_f32 v41, v54, v50, v41 op_sel_hi:[0,1,0]
	v_fma_mix_f32 v44, v54, v50, v44 op_sel:[0,1,0] op_sel_hi:[0,1,0]
	v_fma_mix_f32 v45, v54, v51, v45 op_sel_hi:[0,1,0]
	v_fma_mix_f32 v50, v54, v51, v64 op_sel:[0,1,0] op_sel_hi:[0,1,0]
	v_fma_mix_f32 v51, v54, v52, v65 op_sel_hi:[0,1,0]
	v_fma_mix_f32 v61, v54, v52, v62 op_sel:[0,1,0] op_sel_hi:[0,1,0]
	v_fma_mix_f32 v62, v54, v53, v63 op_sel_hi:[0,1,0]
	v_fma_mix_f32 v54, v54, v53, v60 op_sel:[0,1,0] op_sel_hi:[0,1,0]
	s_waitcnt lgkmcnt(0)
	v_fma_mix_f32 v60, v55, v57, v50 op_sel:[0,1,0] op_sel_hi:[0,1,0]
	v_fma_mix_f32 v63, v55, v58, v51 op_sel_hi:[0,1,0]
	ds_read_b128 v[50:53], v2 offset:57344
	v_fma_mix_f32 v41, v55, v56, v41 op_sel_hi:[0,1,0]
	v_fma_mix_f32 v44, v55, v56, v44 op_sel:[0,1,0] op_sel_hi:[0,1,0]
	v_fma_mix_f32 v45, v55, v57, v45 op_sel_hi:[0,1,0]
	v_fma_mix_f32 v58, v55, v58, v61 op_sel:[0,1,0] op_sel_hi:[0,1,0]
	v_fma_mix_f32 v61, v55, v59, v62 op_sel_hi:[0,1,0]
	v_fma_mix_f32 v59, v55, v59, v54 op_sel:[0,1,0] op_sel_hi:[0,1,0]
	ds_read_b128 v[54:57], v2 offset:61440
	s_waitcnt lgkmcnt(1)
	v_fma_mix_f32 v41, v48, v50, v41 op_sel_hi:[0,1,0]
	v_fma_mix_f32 v44, v48, v50, v44 op_sel:[0,1,0] op_sel_hi:[0,1,0]
	v_fma_mix_f32 v50, v48, v51, v60 op_sel:[0,1,0] op_sel_hi:[0,1,0]
	v_fma_mix_f32 v45, v48, v51, v45 op_sel_hi:[0,1,0]
	v_fma_mix_f32 v51, v48, v52, v63 op_sel_hi:[0,1,0]
	v_fma_mix_f32 v52, v48, v52, v58 op_sel:[0,1,0] op_sel_hi:[0,1,0]
	v_fma_mix_f32 v58, v48, v53, v61 op_sel_hi:[0,1,0]
	v_fma_mix_f32 v48, v48, v53, v59 op_sel:[0,1,0] op_sel_hi:[0,1,0]
	s_waitcnt lgkmcnt(0)
	v_fma_mix_f32 v59, v49, v55, v50 op_sel:[0,1,0] op_sel_hi:[0,1,0]
	v_add_u32_e32 v50, 0x10000, v2
	v_fma_mix_f32 v41, v49, v54, v41 op_sel_hi:[0,1,0]
	v_fma_mix_f32 v44, v49, v54, v44 op_sel:[0,1,0] op_sel_hi:[0,1,0]
	v_fma_mix_f32 v45, v49, v55, v45 op_sel_hi:[0,1,0]
	v_fma_mix_f32 v60, v49, v56, v51 op_sel_hi:[0,1,0]
	v_fma_mix_f32 v61, v49, v56, v52 op_sel:[0,1,0] op_sel_hi:[0,1,0]
	ds_read_b128 v[50:53], v50
	v_fma_mix_f32 v58, v49, v57, v58 op_sel_hi:[0,1,0]
	v_fma_mix_f32 v48, v49, v57, v48 op_sel:[0,1,0] op_sel_hi:[0,1,0]
	v_add_u32_e32 v49, 0x11000, v2
	ds_read_b128 v[54:57], v49
	s_waitcnt lgkmcnt(1)
	v_fma_mix_f32 v44, v46, v50, v44 op_sel:[0,1,0] op_sel_hi:[0,1,0]
	v_fma_mix_f32 v41, v46, v50, v41 op_sel_hi:[0,1,0]
	v_fma_mix_f32 v45, v46, v51, v45 op_sel_hi:[0,1,0]
	v_fma_mix_f32 v49, v46, v51, v59 op_sel:[0,1,0] op_sel_hi:[0,1,0]
	v_fma_mix_f32 v50, v46, v52, v60 op_sel_hi:[0,1,0]
	v_fma_mix_f32 v51, v46, v52, v61 op_sel:[0,1,0] op_sel_hi:[0,1,0]
	v_fma_mix_f32 v52, v46, v53, v58 op_sel_hi:[0,1,0]
	v_fma_mix_f32 v46, v46, v53, v48 op_sel:[0,1,0] op_sel_hi:[0,1,0]
	s_waitcnt lgkmcnt(0)
	v_fma_mix_f32 v53, v47, v54, v44 op_sel:[0,1,0] op_sel_hi:[0,1,0]
	v_add_u32_e32 v44, 0x12000, v2
	v_fma_mix_f32 v41, v47, v54, v41 op_sel_hi:[0,1,0]
	v_fma_mix_f32 v54, v47, v55, v45 op_sel_hi:[0,1,0]
	v_fma_mix_f32 v55, v47, v55, v49 op_sel:[0,1,0] op_sel_hi:[0,1,0]
	v_fma_mix_f32 v58, v47, v56, v50 op_sel_hi:[0,1,0]
	v_fma_mix_f32 v56, v47, v56, v51 op_sel:[0,1,0] op_sel_hi:[0,1,0]
	ds_read_b128 v[48:51], v44
	v_add_u32_e32 v44, 0x13000, v2
	v_fma_mix_f32 v52, v47, v57, v52 op_sel_hi:[0,1,0]
	v_fma_mix_f32 v57, v47, v57, v46 op_sel:[0,1,0] op_sel_hi:[0,1,0]
	ds_read_b128 v[44:47], v44
	s_waitcnt lgkmcnt(1)
	v_fma_mix_f32 v41, v42, v48, v41 op_sel_hi:[0,1,0]
	v_fma_mix_f32 v48, v42, v48, v53 op_sel:[0,1,0] op_sel_hi:[0,1,0]
	v_fma_mix_f32 v53, v42, v49, v54 op_sel_hi:[0,1,0]
	v_fma_mix_f32 v49, v42, v49, v55 op_sel:[0,1,0] op_sel_hi:[0,1,0]
	v_fma_mix_f32 v54, v42, v50, v58 op_sel_hi:[0,1,0]
	v_fma_mix_f32 v50, v42, v50, v56 op_sel:[0,1,0] op_sel_hi:[0,1,0]
	v_fma_mix_f32 v52, v42, v51, v52 op_sel_hi:[0,1,0]
	v_fma_mix_f32 v42, v42, v51, v57 op_sel:[0,1,0] op_sel_hi:[0,1,0]
	s_waitcnt lgkmcnt(0)
	v_fma_mix_f32 v41, v43, v44, v41 op_sel_hi:[0,1,0]
	v_fma_mix_f32 v55, v43, v44, v48 op_sel:[0,1,0] op_sel_hi:[0,1,0]
	v_add_u32_e32 v44, 0x14000, v2
	v_fma_mix_f32 v56, v43, v45, v49 op_sel:[0,1,0] op_sel_hi:[0,1,0]
	v_fma_mix_f32 v54, v43, v46, v54 op_sel_hi:[0,1,0]
	v_fma_mix_f32 v46, v43, v46, v50 op_sel:[0,1,0] op_sel_hi:[0,1,0]
	ds_read_b128 v[48:51], v44
	v_fma_mix_f32 v52, v43, v47, v52 op_sel_hi:[0,1,0]
	v_fma_mix_f32 v47, v43, v47, v42 op_sel:[0,1,0] op_sel_hi:[0,1,0]
	v_add_u32_e32 v42, 0x15000, v2
	v_fma_mix_f32 v53, v43, v45, v53 op_sel_hi:[0,1,0]
	ds_read_b128 v[42:45], v42
	s_waitcnt lgkmcnt(1)
	v_fma_mix_f32 v41, v36, v48, v41 op_sel_hi:[0,1,0]
	v_fma_mix_f32 v48, v36, v48, v55 op_sel:[0,1,0] op_sel_hi:[0,1,0]
	v_fma_mix_f32 v53, v36, v49, v53 op_sel_hi:[0,1,0]
	v_fma_mix_f32 v49, v36, v49, v56 op_sel:[0,1,0] op_sel_hi:[0,1,0]
	v_fma_mix_f32 v54, v36, v50, v54 op_sel_hi:[0,1,0]
	v_fma_mix_f32 v46, v36, v50, v46 op_sel:[0,1,0] op_sel_hi:[0,1,0]
	v_fma_mix_f32 v50, v36, v51, v52 op_sel_hi:[0,1,0]
	v_fma_mix_f32 v36, v36, v51, v47 op_sel:[0,1,0] op_sel_hi:[0,1,0]
	s_waitcnt lgkmcnt(0)
	v_fma_mix_f32 v41, v37, v42, v41 op_sel_hi:[0,1,0]
	v_fma_mix_f32 v51, v37, v42, v48 op_sel:[0,1,0] op_sel_hi:[0,1,0]
	v_add_u32_e32 v42, 0x16000, v2
	v_fma_mix_f32 v52, v37, v43, v53 op_sel_hi:[0,1,0]
	v_fma_mix_f32 v53, v37, v43, v49 op_sel:[0,1,0] op_sel_hi:[0,1,0]
	v_fma_mix_f32 v54, v37, v44, v54 op_sel_hi:[0,1,0]
	v_fma_mix_f32 v55, v37, v44, v46 op_sel:[0,1,0] op_sel_hi:[0,1,0]
	ds_read_b128 v[46:49], v42
	v_fma_mix_f32 v50, v37, v45, v50 op_sel_hi:[0,1,0]
	v_fma_mix_f32 v36, v37, v45, v36 op_sel:[0,1,0] op_sel_hi:[0,1,0]
	v_add_u32_e32 v37, 0x17000, v2
	ds_read_b128 v[42:45], v37
	s_waitcnt lgkmcnt(1)
	v_fma_mix_f32 v37, v14, v46, v41 op_sel_hi:[0,1,0]
	v_fma_mix_f32 v41, v14, v46, v51 op_sel:[0,1,0] op_sel_hi:[0,1,0]
	v_fma_mix_f32 v46, v14, v47, v52 op_sel_hi:[0,1,0]
	v_fma_mix_f32 v47, v14, v47, v53 op_sel:[0,1,0] op_sel_hi:[0,1,0]
	v_fma_mix_f32 v51, v14, v48, v54 op_sel_hi:[0,1,0]
	v_fma_mix_f32 v48, v14, v48, v55 op_sel:[0,1,0] op_sel_hi:[0,1,0]
	v_fma_mix_f32 v50, v14, v49, v50 op_sel_hi:[0,1,0]
	v_fma_mix_f32 v14, v14, v49, v36 op_sel:[0,1,0] op_sel_hi:[0,1,0]
	s_waitcnt lgkmcnt(0)
	v_fma_mix_f32 v36, v15, v42, v37 op_sel_hi:[0,1,0]
	v_fma_mix_f32 v37, v15, v42, v41 op_sel:[0,1,0] op_sel_hi:[0,1,0]
	v_add_u32_e32 v42, 0x18000, v2
	v_fma_mix_f32 v41, v15, v43, v46 op_sel_hi:[0,1,0]
	v_fma_mix_f32 v52, v15, v43, v47 op_sel:[0,1,0] op_sel_hi:[0,1,0]
	v_fma_mix_f32 v51, v15, v44, v51 op_sel_hi:[0,1,0]
	v_fma_mix_f32 v53, v15, v44, v48 op_sel:[0,1,0] op_sel_hi:[0,1,0]
	ds_read_b128 v[46:49], v42
	v_fma_mix_f32 v50, v15, v45, v50 op_sel_hi:[0,1,0]
	v_fma_mix_f32 v14, v15, v45, v14 op_sel:[0,1,0] op_sel_hi:[0,1,0]
	v_add_u32_e32 v15, 0x19000, v2
	ds_read_b128 v[42:45], v15
	s_waitcnt lgkmcnt(1)
	v_fma_mix_f32 v15, v6, v46, v36 op_sel_hi:[0,1,0]
	v_fma_mix_f32 v36, v6, v46, v37 op_sel:[0,1,0] op_sel_hi:[0,1,0]
	v_fma_mix_f32 v37, v6, v47, v41 op_sel_hi:[0,1,0]
	v_fma_mix_f32 v41, v6, v47, v52 op_sel:[0,1,0] op_sel_hi:[0,1,0]
	v_fma_mix_f32 v46, v6, v48, v51 op_sel_hi:[0,1,0]
	v_fma_mix_f32 v47, v6, v48, v53 op_sel:[0,1,0] op_sel_hi:[0,1,0]
	v_fma_mix_f32 v50, v6, v49, v50 op_sel_hi:[0,1,0]
	v_fma_mix_f32 v6, v6, v49, v14 op_sel:[0,1,0] op_sel_hi:[0,1,0]
	s_waitcnt lgkmcnt(0)
	v_fma_mix_f32 v14, v7, v42, v15 op_sel_hi:[0,1,0]
	v_fma_mix_f32 v15, v7, v42, v36 op_sel:[0,1,0] op_sel_hi:[0,1,0]
	v_add_u32_e32 v42, 0x1a000, v2
	v_fma_mix_f32 v36, v7, v43, v37 op_sel_hi:[0,1,0]
	v_fma_mix_f32 v37, v7, v43, v41 op_sel:[0,1,0] op_sel_hi:[0,1,0]
	v_fma_mix_f32 v41, v7, v44, v46 op_sel_hi:[0,1,0]
	v_fma_mix_f32 v51, v7, v44, v47 op_sel:[0,1,0] op_sel_hi:[0,1,0]
	ds_read_b128 v[46:49], v42
	v_fma_mix_f32 v50, v7, v45, v50 op_sel_hi:[0,1,0]
	v_fma_mix_f32 v6, v7, v45, v6 op_sel:[0,1,0] op_sel_hi:[0,1,0]
	v_add_u32_e32 v7, 0x1b000, v2
	ds_read_b128 v[42:45], v7
	s_waitcnt lgkmcnt(1)
	v_fma_mix_f32 v7, v4, v46, v14 op_sel_hi:[0,1,0]
	v_fma_mix_f32 v14, v4, v46, v15 op_sel:[0,1,0] op_sel_hi:[0,1,0]
	v_fma_mix_f32 v15, v4, v47, v36 op_sel_hi:[0,1,0]
	v_fma_mix_f32 v36, v4, v47, v37 op_sel:[0,1,0] op_sel_hi:[0,1,0]
	v_fma_mix_f32 v37, v4, v48, v41 op_sel_hi:[0,1,0]
	v_fma_mix_f32 v41, v4, v48, v51 op_sel:[0,1,0] op_sel_hi:[0,1,0]
	v_fma_mix_f32 v50, v4, v49, v50 op_sel_hi:[0,1,0]
	v_fma_mix_f32 v4, v4, v49, v6 op_sel:[0,1,0] op_sel_hi:[0,1,0]
	s_waitcnt lgkmcnt(0)
	v_fma_mix_f32 v6, v5, v42, v7 op_sel_hi:[0,1,0]
	v_fma_mix_f32 v7, v5, v42, v14 op_sel:[0,1,0] op_sel_hi:[0,1,0]
	v_fma_mix_f32 v14, v5, v43, v15 op_sel_hi:[0,1,0]
	v_fma_mix_f32 v15, v5, v43, v36 op_sel:[0,1,0] op_sel_hi:[0,1,0]
	v_fma_mix_f32 v36, v5, v44, v37 op_sel_hi:[0,1,0]
	v_fma_mix_f32 v37, v5, v44, v41 op_sel:[0,1,0] op_sel_hi:[0,1,0]
	v_add_u32_e32 v41, 0x1c000, v2
	ds_read_b128 v[46:49], v41
	v_fma_mix_f32 v41, v5, v45, v50 op_sel_hi:[0,1,0]
	v_fma_mix_f32 v4, v5, v45, v4 op_sel:[0,1,0] op_sel_hi:[0,1,0]
	v_add_u32_e32 v5, 0x1d000, v2
	ds_read_b128 v[42:45], v5
	s_waitcnt lgkmcnt(1)
	v_fma_mix_f32 v5, v12, v46, v6 op_sel_hi:[0,1,0]
	v_fma_mix_f32 v6, v12, v46, v7 op_sel:[0,1,0] op_sel_hi:[0,1,0]
	v_fma_mix_f32 v7, v12, v47, v14 op_sel_hi:[0,1,0]
	v_fma_mix_f32 v14, v12, v47, v15 op_sel:[0,1,0] op_sel_hi:[0,1,0]
	v_fma_mix_f32 v15, v12, v48, v36 op_sel_hi:[0,1,0]
	s_waitcnt lgkmcnt(0)
	v_fma_mix_f32 v55, v13, v44, v15 op_sel_hi:[0,1,0]
	v_lshlrev_b32_e32 v15, 5, v1
	v_fma_mix_f32 v36, v12, v48, v37 op_sel:[0,1,0] op_sel_hi:[0,1,0]
	v_fma_mix_f32 v37, v12, v49, v41 op_sel_hi:[0,1,0]
	v_fma_mix_f32 v12, v12, v49, v4 op_sel:[0,1,0] op_sel_hi:[0,1,0]
	v_fma_mix_f32 v41, v13, v42, v5 op_sel_hi:[0,1,0]
	v_fma_mix_f32 v42, v13, v42, v6 op_sel:[0,1,0] op_sel_hi:[0,1,0]
	v_fma_mix_f32 v54, v13, v43, v7 op_sel_hi:[0,1,0]
	global_load_dwordx4 v[4:7], v15, s[88:89] offset:16 nt
	global_load_dwordx4 v[46:49], v15, s[88:89] nt
	v_fma_mix_f32 v43, v13, v43, v14 op_sel:[0,1,0] op_sel_hi:[0,1,0]
	v_add_u32_e32 v14, 0x1e000, v2
	ds_read_b128 v[50:53], v14
	v_add_u32_e32 v2, 0x1f000, v2
	v_fma_mix_f32 v36, v13, v44, v36 op_sel:[0,1,0] op_sel_hi:[0,1,0]
	v_fma_mix_f32 v37, v13, v45, v37 op_sel_hi:[0,1,0]
	v_fma_mix_f32 v44, v13, v45, v12 op_sel:[0,1,0] op_sel_hi:[0,1,0]
	ds_read_b128 v[12:15], v2
	s_waitcnt lgkmcnt(1)
	v_fma_mix_f32 v2, v10, v50, v41 op_sel_hi:[0,1,0]
	v_fma_mix_f32 v41, v10, v50, v42 op_sel:[0,1,0] op_sel_hi:[0,1,0]
	v_fma_mix_f32 v42, v10, v51, v54 op_sel_hi:[0,1,0]
	v_fma_mix_f32 v43, v10, v51, v43 op_sel:[0,1,0] op_sel_hi:[0,1,0]
	v_fma_mix_f32 v45, v10, v52, v55 op_sel_hi:[0,1,0]
	v_fma_mix_f32 v36, v10, v52, v36 op_sel:[0,1,0] op_sel_hi:[0,1,0]
	v_fma_mix_f32 v37, v10, v53, v37 op_sel_hi:[0,1,0]
	v_fma_mix_f32 v10, v10, v53, v44 op_sel:[0,1,0] op_sel_hi:[0,1,0]
	s_waitcnt lgkmcnt(0)
	v_fma_mix_f32 v2, v11, v12, v2 op_sel_hi:[0,1,0]
	v_fma_mix_f32 v12, v11, v12, v41 op_sel:[0,1,0] op_sel_hi:[0,1,0]
	v_fma_mix_f32 v41, v11, v13, v42 op_sel_hi:[0,1,0]
	v_fma_mix_f32 v13, v11, v13, v43 op_sel:[0,1,0] op_sel_hi:[0,1,0]
	v_fma_mix_f32 v42, v11, v14, v45 op_sel_hi:[0,1,0]
	v_fma_mix_f32 v14, v11, v14, v36 op_sel:[0,1,0] op_sel_hi:[0,1,0]
	v_fma_mix_f32 v36, v11, v15, v37 op_sel_hi:[0,1,0]
	v_fma_mix_f32 v10, v11, v15, v10 op_sel:[0,1,0] op_sel_hi:[0,1,0]
	v_cndmask_b32_e64 v11, v41, v13, s[0:1]
	v_cndmask_b32_e64 v43, v2, v12, s[0:1]
	v_cndmask_b32_e64 v2, v12, v2, s[0:1]
	v_cndmask_b32_e64 v12, v13, v41, s[0:1]
	ds_bpermute_b32 v11, v85, v11
	v_cndmask_b32_e64 v13, v42, v14, s[0:1]
	v_cndmask_b32_e64 v15, v36, v10, s[0:1]
	ds_bpermute_b32 v43, v85, v43
	ds_bpermute_b32 v13, v85, v13
	ds_bpermute_b32 v15, v85, v15
	s_waitcnt lgkmcnt(3)
	v_add_f32_e32 v11, v12, v11
	v_cndmask_b32_e64 v12, v14, v42, s[0:1]
	v_cndmask_b32_e64 v10, v10, v36, s[0:1]
	s_waitcnt lgkmcnt(2)
	v_add_f32_e32 v2, v2, v43
	s_waitcnt lgkmcnt(1)
	v_add_f32_e32 v12, v12, v13
	s_waitcnt lgkmcnt(0)
	v_add_f32_e32 v10, v10, v15
	v_cndmask_b32_e64 v13, v2, v11, s[2:3]
	v_cndmask_b32_e64 v14, v12, v10, s[2:3]
	ds_bpermute_b32 v13, v84, v13
	ds_bpermute_b32 v14, v84, v14
	v_cndmask_b32_e64 v2, v11, v2, s[2:3]
	v_cndmask_b32_e64 v10, v10, v12, s[2:3]
	s_waitcnt lgkmcnt(1)
	v_add_f32_e32 v2, v2, v13
	s_waitcnt lgkmcnt(0)
	v_add_f32_e32 v10, v10, v14
	v_cndmask_b32_e64 v11, v2, v10, s[4:5]
	ds_bpermute_b32 v11, v83, v11
	v_cndmask_b32_e64 v2, v10, v2, s[4:5]
	s_waitcnt lgkmcnt(0)
	v_add_f32_e32 v2, v2, v11
	ds_bpermute_b32 v10, v82, v2
	s_waitcnt lgkmcnt(0)
	v_add_f32_e32 v2, v2, v10
	ds_bpermute_b32 v10, v34, v2
	s_waitcnt lgkmcnt(0)
	v_add_f32_e32 v2, v2, v10
	ds_bpermute_b32 v9, v9, v2
	s_waitcnt lgkmcnt(0)
	v_add_f32_e32 v2, v2, v9
	s_nop 0
	v_readlane_b32 s8, v2, 0
	v_readlane_b32 s9, v2, 32
	v_readlane_b32 s10, v2, 16
	v_readlane_b32 s11, v2, 48
	v_readlane_b32 s12, v2, 8
	s_waitcnt vmcnt(0)
	v_pk_fma_f32 v[10:11], v[8:9], s[8:9], v[46:47] op_sel_hi:[0,1,1]
	v_cmp_gt_f32_e64 s[8:9], v11, v10
	v_readlane_b32 s13, v2, 40
	v_readlane_b32 s14, v2, 24
	v_readlane_b32 s15, v2, 56
	v_fma_f32 v9, s10, v8, v48
	v_cndmask_b32_e64 v2, v10, v11, s[8:9]
	v_fma_f32 v12, s13, v8, v5
	v_cndmask_b32_e64 v5, 0, 1, s[8:9]
	v_cmp_gt_f32_e64 s[8:9], v9, v2
	v_fmac_f32_e32 v49, s11, v8
	v_fma_f32 v4, s12, v8, v4
	v_cndmask_b32_e64 v2, v2, v9, s[8:9]
	v_cndmask_b32_e64 v5, v5, 2, s[8:9]
	v_cmp_gt_f32_e64 s[8:9], v49, v2
	v_fma_f32 v6, s14, v8, v6
	v_fmac_f32_e32 v7, s15, v8
	v_cndmask_b32_e64 v2, v2, v49, s[8:9]
	v_cndmask_b32_e64 v5, v5, 3, s[8:9]
	v_cmp_gt_f32_e64 s[8:9], v4, v2
	v_cmp_nlt_f32_e64 s[16:17], s54, v10
	s_nop 0
	v_cndmask_b32_e64 v2, v2, v4, s[8:9]
	v_cndmask_b32_e64 v5, v5, 4, s[8:9]
	v_cmp_gt_f32_e64 s[8:9], v12, v2
	s_nop 1
	v_cndmask_b32_e64 v2, v2, v12, s[8:9]
	v_cndmask_b32_e64 v8, v5, 5, s[8:9]
	v_cmp_ngt_f32_e64 s[8:9], v6, v2
	s_nop 1
	v_cndmask_b32_e64 v5, v6, v2, s[8:9]
	v_cndmask_b32_e64 v2, 6, v8, s[8:9]
	v_cmp_gt_f32_e64 s[12:13], v7, v5
	v_cmp_ngt_f32_e64 s[10:11], v7, v5
	s_nop 0
	v_cndmask_b32_e64 v2, v2, 7, s[12:13]
	v_cmp_eq_u32_e64 s[14:15], 0, v2
	s_or_b64 s[14:15], s[14:15], s[16:17]
	s_or_b64 s[12:13], s[8:9], s[12:13]
	v_cndmask_b32_e64 v8, v10, v81, s[14:15]
	v_cndmask_b32_e64 v10, 0, -1, s[14:15]
	v_cmp_ne_u32_e64 s[14:15], 1, v2
	v_cmp_gt_f32_e64 s[16:17], v11, v8
	s_and_b64 s[14:15], s[14:15], s[16:17]
	v_cndmask_b32_e64 v8, v8, v11, s[14:15]
	v_cndmask_b32_e64 v10, v10, 1, s[14:15]
	v_cmp_ne_u32_e64 s[14:15], 2, v2
	v_cmp_gt_f32_e64 s[16:17], v9, v8
	s_and_b64 s[14:15], s[14:15], s[16:17]
	v_cndmask_b32_e64 v8, v8, v9, s[14:15]
	v_cndmask_b32_e64 v9, v10, 2, s[14:15]
	v_cmp_ne_u32_e64 s[14:15], 3, v2
	v_cmp_gt_f32_e64 s[16:17], v49, v8
	s_and_b64 s[14:15], s[14:15], s[16:17]
	v_cndmask_b32_e64 v8, v8, v49, s[14:15]
	v_cndmask_b32_e64 v9, v9, 3, s[14:15]
	v_cmp_ne_u32_e64 s[14:15], 4, v2
	v_cmp_gt_f32_e64 s[16:17], v4, v8
	s_and_b64 s[14:15], s[14:15], s[16:17]
	v_cndmask_b32_e64 v4, v8, v4, s[14:15]
	v_cndmask_b32_e64 v8, v9, 4, s[14:15]
	v_cmp_ne_u32_e64 s[14:15], 5, v2
	v_cmp_gt_f32_e64 s[16:17], v12, v4
	s_and_b64 s[14:15], s[14:15], s[16:17]
	v_cndmask_b32_e64 v4, v4, v12, s[14:15]
	v_cmp_gt_f32_e64 s[8:9], v6, v4
	v_cndmask_b32_e64 v8, v8, 5, s[14:15]
	s_and_b64 s[8:9], s[12:13], s[8:9]
	v_cndmask_b32_e64 v4, v4, v6, s[8:9]
	v_cndmask_b32_e64 v6, v8, 6, s[8:9]
	s_and_saveexec_b64 s[12:13], s[10:11]
	s_cbranch_execz .LBB0_548
	v_cmp_gt_f32_e64 s[8:9], v7, v4
	s_and_saveexec_b64 s[10:11], s[8:9]
	v_mov_b32_e32 v6, 7
	v_mov_b32_e32 v4, v7
	s_or_b64 exec, exec, s[10:11]
	v_mov_b32_e32 v7, v5

.LBB0_1411:
	v_readlane_b32 s2, v250, 5
	s_mov_b32 s26, 0
	s_cmpk_gt_i32 s24, 0x41ff
	v_add_u32_e32 v16, s2, v76
	v_ashrrev_i32_e32 v17, 31, v16
	v_lshl_add_u64 v[66:67], v[16:17], 4, s[74:75]
	v_add_co_u32_e32 v8, vcc, 0xd40000, v66
	v_lshl_add_u32 v17, v16, 4, 0
	s_nop 0
	v_addc_co_u32_e32 v9, vcc, 0, v67, vcc
	v_add_co_u32_e32 v10, vcc, 0xd42000, v66
	v_readlane_b32 s3, v250, 6
	s_nop 0
	v_addc_co_u32_e32 v11, vcc, 0, v67, vcc
	v_add_co_u32_e32 v18, vcc, 0xd44000, v66
	global_load_dwordx4 v[0:3], v[8:9], off nt
	global_load_dwordx4 v[4:7], v[10:11], off nt
	v_addc_co_u32_e32 v19, vcc, 0, v67, vcc
	v_add_co_u32_e32 v20, vcc, 0xd46000, v66
	s_nop 1
	v_addc_co_u32_e32 v21, vcc, 0, v67, vcc
	v_add_co_u32_e32 v26, vcc, 0xd48000, v66
	global_load_dwordx4 v[8:11], v[18:19], off nt
	global_load_dwordx4 v[12:15], v[20:21], off nt
	v_addc_co_u32_e32 v27, vcc, 0, v67, vcc
	v_add_co_u32_e32 v28, vcc, 0xd4a000, v66
	s_nop 1
	v_addc_co_u32_e32 v29, vcc, 0, v67, vcc
	v_add_co_u32_e32 v34, vcc, 0xd4c000, v66
	global_load_dwordx4 v[18:21], v[26:27], off nt
	global_load_dwordx4 v[22:25], v[28:29], off nt
	v_addc_co_u32_e32 v35, vcc, 0, v67, vcc
	v_add_co_u32_e32 v36, vcc, 0xd4e000, v66
	s_nop 1
	v_addc_co_u32_e32 v37, vcc, 0, v67, vcc
	v_add_co_u32_e32 v42, vcc, 0xd50000, v66
	global_load_dwordx4 v[26:29], v[34:35], off nt
	global_load_dwordx4 v[30:33], v[36:37], off nt
	v_addc_co_u32_e32 v43, vcc, 0, v67, vcc
	v_add_co_u32_e32 v44, vcc, 0xd52000, v66
	s_nop 1
	v_addc_co_u32_e32 v45, vcc, 0, v67, vcc
	v_add_co_u32_e32 v50, vcc, 0xd54000, v66
	global_load_dwordx4 v[34:37], v[42:43], off nt
	global_load_dwordx4 v[38:41], v[44:45], off nt
	v_addc_co_u32_e32 v51, vcc, 0, v67, vcc
	v_add_co_u32_e32 v52, vcc, 0xd56000, v66
	s_nop 1
	v_addc_co_u32_e32 v53, vcc, 0, v67, vcc
	v_add_co_u32_e32 v58, vcc, 0xd58000, v66
	global_load_dwordx4 v[42:45], v[50:51], off nt
	global_load_dwordx4 v[46:49], v[52:53], off nt
	v_addc_co_u32_e32 v59, vcc, 0, v67, vcc
	v_add_co_u32_e32 v60, vcc, 0xd5a000, v66
	s_nop 1
	v_addc_co_u32_e32 v61, vcc, 0, v67, vcc
	v_add_co_u32_e32 v68, vcc, 0xd5c000, v66
	global_load_dwordx4 v[50:53], v[58:59], off nt
	global_load_dwordx4 v[54:57], v[60:61], off nt
	v_addc_co_u32_e32 v69, vcc, 0, v67, vcc
	v_add_co_u32_e32 v70, vcc, 0xd5e000, v66
	s_nop 1
	v_addc_co_u32_e32 v71, vcc, 0, v67, vcc
	v_add_co_u32_e32 v74, vcc, 0xd04000, v66
	global_load_dwordx4 v[58:61], v[68:69], off nt
	global_load_dwordx4 v[62:65], v[70:71], off nt
	v_addc_co_u32_e32 v75, vcc, 0, v67, vcc
	v_add_co_u32_e32 v78, vcc, 0xd06000, v66
	s_nop 1
	v_addc_co_u32_e32 v79, vcc, 0, v67, vcc
	global_load_dwordx4 v[66:69], v[74:75], off nt
	global_load_dwordx4 v[70:73], v[78:79], off nt
	s_waitcnt vmcnt(17)
	ds_write_b128 v17, v[0:3]
	s_waitcnt vmcnt(16)
	ds_write_b128 v17, v[4:7] offset:8192
	s_waitcnt vmcnt(15)
	ds_write_b128 v17, v[8:11] offset:16384
	s_waitcnt vmcnt(14)
	ds_write_b128 v17, v[12:15] offset:24576
	s_waitcnt vmcnt(13)
	ds_write_b128 v17, v[18:21] offset:32768
	s_waitcnt vmcnt(12)
	ds_write_b128 v17, v[22:25] offset:40960
	s_waitcnt vmcnt(11)
	ds_write_b128 v17, v[26:29] offset:49152
	s_waitcnt vmcnt(10)
	ds_write_b128 v17, v[30:33] offset:57344
	v_add_u32_e32 v0, 0x10000, v17
	s_waitcnt vmcnt(9)
	ds_write_b128 v0, v[34:37]
	v_add_u32_e32 v0, 0x12000, v17
	s_waitcnt vmcnt(8)
	ds_write_b128 v0, v[38:41]
	v_add_u32_e32 v0, 0x14000, v17
	s_waitcnt vmcnt(7)
	ds_write_b128 v0, v[42:45]
	v_add_u32_e32 v0, 0x16000, v17
	s_waitcnt vmcnt(6)
	ds_write_b128 v0, v[46:49]
	v_add_u32_e32 v0, 0x18000, v17
	s_waitcnt vmcnt(5)
	ds_write_b128 v0, v[50:53]
	v_add_u32_e32 v0, 0x1a000, v17
	s_waitcnt vmcnt(4)
	ds_write_b128 v0, v[54:57]
	v_add_u32_e32 v0, 0x1c000, v17
	s_waitcnt vmcnt(3)
	ds_write_b128 v0, v[58:61]
	v_add_u32_e32 v0, 0x1e000, v17
	s_waitcnt vmcnt(2)
	ds_write_b128 v0, v[62:65]
	v_add_u32_e32 v0, 0x20800, v17
	s_waitcnt vmcnt(1)
	ds_write_b128 v0, v[66:69]
	s_waitcnt vmcnt(0)
	ds_write_b128 v0, v[70:73] offset:8192
	s_waitcnt lgkmcnt(0)
	s_barrier
	s_cbranch_scc1 .LBB0_1433
	s_add_u32 s33, s74, 0x27a00000
	s_addc_u32 s42, s75, 0
	v_and_b32_e32 v0, 32, v76
	s_add_u32 s20, s74, 0x9000
	v_lshlrev_b32_e32 v18, 2, v76
	v_cmp_eq_u32_e64 s[2:3], 0, v0
	v_and_b32_e32 v0, 16, v76
	v_readlane_b32 s52, v250, 7
	s_addc_u32 s21, s75, 0
	v_ashrrev_i32_e32 v19, 31, v18
	v_cmp_eq_u32_e64 s[68:69], 0, v0
	v_and_b32_e32 v0, 8, v76
	v_readlane_b32 s58, v250, 13
	v_readlane_b32 s59, v250, 14
	s_add_u32 s43, s74, 0x100000
	v_cmp_eq_u32_e64 s[70:71], 0, v0
	v_lshl_add_u64 v[0:1], v[18:19], 2, s[58:59]
	s_mov_b64 s[10:11], 0x2000
	s_addc_u32 s44, s75, 0
	v_lshl_add_u64 v[22:23], v[0:1], 0, s[10:11]
	s_mov_b64 s[10:11], 0x3000
	s_add_u32 s45, s74, 0x140000
	v_lshl_add_u64 v[24:25], v[0:1], 0, s[10:11]
	s_mov_b64 s[10:11], 0x3400
	s_addc_u32 s46, s75, 0
	v_lshl_add_u64 v[26:27], v[0:1], 0, s[10:11]
	s_mov_b64 s[10:11], 0x3800
	s_add_u32 s28, s74, 0x3c400000
	v_lshl_add_u64 v[28:29], v[0:1], 0, s[10:11]
	s_mov_b64 s[10:11], 0x3c00
	s_addc_u32 s29, s75, 0
	v_readlane_b32 s53, v250, 8
	v_readlane_b32 s54, v250, 9
	v_readlane_b32 s55, v250, 10
	v_readlane_b32 s56, v250, 11
	v_readlane_b32 s57, v250, 12
	v_readlane_b32 s60, v250, 15
	v_readlane_b32 s67, v250, 22
	v_lshl_add_u64 v[30:31], v[0:1], 0, s[10:11]
	s_add_u32 s30, s74, 0x3c700000
	v_mbcnt_lo_u32_b32 v0, -1, 0
	v_lshl_add_u64 v[20:21], v[18:19], 1, s[96:97]
	v_cmp_eq_u32_e64 s[76:77], 0, v76
	s_mov_b32 s60, s78
	v_readlane_b32 s67, v250, 53
	s_addc_u32 s31, s75, 0
	s_movk_i32 s47, 0x1000
	s_mov_b64 s[34:35], 0x400000
	s_mov_b32 s48, 0x401000
	s_mov_b64 s[36:37], 0x800000
	s_mov_b32 s49, 0x801000
	s_mov_b64 s[38:39], 0xc00000
	s_mov_b32 s52, 0xc01000
	v_mov_b32_e32 v17, 0x358637bd
	v_mov_b32_e32 v33, 0
	s_mov_b32 s53, 0xff61b1e6
	s_add_i32 s54, 0, 0x24900
	s_movk_i32 s55, 0x9f
	s_movk_i32 s56, 0x4200
	s_add_i32 s57, 0, 0x24800
	v_mov_b32_e32 v77, 1
	v_mbcnt_hi_u32_b32 v78, -1, v0
	v_mov_b32_e32 v79, 0xff61b1e6
	v_readlane_b32 s61, v250, 16
	v_readlane_b32 s62, v250, 17
	v_readlane_b32 s63, v250, 18
	v_readlane_b32 s64, v250, 19
	v_readlane_b32 s65, v250, 20
	v_readlane_b32 s66, v250, 21
	s_branch .LBB0_1414

.LBB0_1418:
	s_add_u32 s12, s14, s12
	s_addc_u32 s13, s15, s13
	v_lshl_add_u64 v[68:69], v[18:19], 2, s[12:13]
	v_add_co_u32_e32 v168, vcc, s47, v68
	v_lshl_add_u64 v[108:109], v[68:69], 0, s[34:35]
	s_nop 0
	v_addc_co_u32_e32 v169, vcc, 0, v69, vcc
	v_add_co_u32_e32 v172, vcc, s48, v68
	v_lshl_add_u64 v[112:113], v[68:69], 0, s[36:37]
	s_nop 0
	v_addc_co_u32_e32 v173, vcc, 0, v69, vcc
	v_add_co_u32_e32 v176, vcc, s49, v68
	v_lshl_add_u64 v[116:117], v[68:69], 0, s[38:39]
	s_nop 0
	v_addc_co_u32_e32 v177, vcc, 0, v69, vcc
	v_add_co_u32_e32 v180, vcc, s52, v68
	global_load_dwordx4 v[12:15], v[68:69], off nt
	global_load_dwordx4 v[8:11], v[68:69], off offset:1024 nt
	global_load_dwordx4 v[4:7], v[68:69], off offset:2048 nt
	global_load_dwordx4 v[0:3], v[68:69], off offset:3072 nt
	v_addc_co_u32_e32 v181, vcc, 0, v69, vcc
	global_load_dwordx4 v[68:71], v[172:173], off offset:-4096 nt
	global_load_dwordx4 v[72:75], v[176:177], off offset:-4096 nt
	global_load_dwordx4 v[80:83], v[180:181], off offset:-4096 nt
	global_load_dwordx4 v[84:87], v[108:109], off offset:1024 nt
	global_load_dwordx4 v[88:91], v[112:113], off offset:1024 nt
	global_load_dwordx4 v[92:95], v[116:117], off offset:1024 nt
	global_load_dwordx4 v[96:99], v[108:109], off offset:2048 nt
	global_load_dwordx4 v[100:103], v[112:113], off offset:2048 nt
	global_load_dwordx4 v[104:107], v[116:117], off offset:2048 nt
	s_nop 0
	global_load_dwordx4 v[108:111], v[108:109], off offset:3072 nt
	s_nop 0
	global_load_dwordx4 v[112:115], v[112:113], off offset:3072 nt
	s_nop 0
	global_load_dwordx4 v[116:119], v[116:117], off offset:3072 nt
	s_nop 0
	global_load_dwordx4 v[120:123], v[168:169], off nt
	global_load_dwordx4 v[124:127], v[172:173], off nt
	global_load_dwordx4 v[128:131], v[176:177], off nt
	global_load_dwordx4 v[132:135], v[180:181], off nt
	global_load_dwordx4 v[136:139], v[168:169], off offset:1024 nt
	global_load_dwordx4 v[140:143], v[172:173], off offset:1024 nt
	global_load_dwordx4 v[144:147], v[176:177], off offset:1024 nt
	global_load_dwordx4 v[148:151], v[180:181], off offset:1024 nt
	global_load_dwordx4 v[152:155], v[168:169], off offset:2048 nt
	global_load_dwordx4 v[156:159], v[172:173], off offset:2048 nt
	global_load_dwordx4 v[160:163], v[176:177], off offset:2048 nt
	global_load_dwordx4 v[164:167], v[180:181], off offset:2048 nt
	s_nop 0
	global_load_dwordx4 v[168:171], v[168:169], off offset:3072 nt
	s_nop 0
	global_load_dwordx4 v[172:175], v[172:173], off offset:3072 nt
	s_nop 0
	global_load_dwordx4 v[176:179], v[176:177], off offset:3072 nt
	s_nop 0
	global_load_dwordx4 v[180:183], v[180:181], off offset:3072 nt
	v_cndmask_b32_e64 v32, 0, 1, s[10:11]
	v_cmp_ne_u32_e32 vcc, 1, v32
	s_mov_b64 s[10:11], 0
	s_mov_b64 s[12:13], 0x1000000
	s_and_b64 vcc, exec, vcc
	s_waitcnt vmcnt(27)
	v_pk_add_f32 v[14:15], v[14:15], v[70:71]
	v_pk_add_f32 v[12:13], v[12:13], v[68:69]
	s_waitcnt vmcnt(25)
	v_pk_add_f32 v[68:69], v[74:75], v[82:83]
	v_pk_add_f32 v[70:71], v[72:73], v[80:81]
	s_waitcnt vmcnt(24)
	v_pk_add_f32 v[10:11], v[10:11], v[86:87]
	v_pk_add_f32 v[8:9], v[8:9], v[84:85]
	s_waitcnt vmcnt(22)
	v_pk_add_f32 v[72:73], v[90:91], v[94:95]
	v_pk_add_f32 v[74:75], v[88:89], v[92:93]
	s_waitcnt vmcnt(21)
	v_pk_add_f32 v[6:7], v[6:7], v[98:99]
	v_pk_add_f32 v[4:5], v[4:5], v[96:97]
	s_waitcnt vmcnt(19)
	v_pk_add_f32 v[80:81], v[102:103], v[106:107]
	v_pk_add_f32 v[82:83], v[100:101], v[104:105]
	s_waitcnt vmcnt(18)
	v_pk_add_f32 v[2:3], v[2:3], v[110:111]
	v_pk_add_f32 v[0:1], v[0:1], v[108:109]
	s_waitcnt vmcnt(16)
	v_pk_add_f32 v[84:85], v[114:115], v[118:119]
	v_pk_add_f32 v[86:87], v[112:113], v[116:117]
	s_waitcnt vmcnt(14)
	v_pk_add_f32 v[88:89], v[122:123], v[126:127]
	v_pk_add_f32 v[90:91], v[120:121], v[124:125]
	s_waitcnt vmcnt(12)
	v_pk_add_f32 v[92:93], v[130:131], v[134:135]
	v_pk_add_f32 v[94:95], v[128:129], v[132:133]
	s_waitcnt vmcnt(10)
	v_pk_add_f32 v[96:97], v[138:139], v[142:143]
	v_pk_add_f32 v[98:99], v[136:137], v[140:141]
	s_waitcnt vmcnt(8)
	v_pk_add_f32 v[100:101], v[146:147], v[150:151]
	v_pk_add_f32 v[102:103], v[144:145], v[148:149]
	s_waitcnt vmcnt(6)
	v_pk_add_f32 v[104:105], v[154:155], v[158:159]
	v_pk_add_f32 v[106:107], v[152:153], v[156:157]
	s_waitcnt vmcnt(4)
	v_pk_add_f32 v[108:109], v[162:163], v[166:167]
	v_pk_add_f32 v[110:111], v[160:161], v[164:165]
	s_waitcnt vmcnt(2)
	v_pk_add_f32 v[112:113], v[170:171], v[174:175]
	v_pk_add_f32 v[114:115], v[168:169], v[172:173]
	s_waitcnt vmcnt(0)
	v_pk_add_f32 v[116:117], v[178:179], v[182:183]
	v_pk_add_f32 v[118:119], v[176:177], v[180:181]
	v_pk_add_f32 v[14:15], v[14:15], v[68:69]
	v_pk_add_f32 v[12:13], v[12:13], v[70:71]
	v_pk_add_f32 v[10:11], v[10:11], v[72:73]
	v_pk_add_f32 v[8:9], v[8:9], v[74:75]
	v_pk_add_f32 v[6:7], v[6:7], v[80:81]
	v_pk_add_f32 v[4:5], v[4:5], v[82:83]
	v_pk_add_f32 v[2:3], v[2:3], v[84:85]
	v_pk_add_f32 v[0:1], v[0:1], v[86:87]
	v_pk_add_f32 v[68:69], v[88:89], v[92:93]
	v_pk_add_f32 v[70:71], v[90:91], v[94:95]
	v_pk_add_f32 v[72:73], v[96:97], v[100:101]
	v_pk_add_f32 v[74:75], v[98:99], v[102:103]
	v_pk_add_f32 v[80:81], v[104:105], v[108:109]
	v_pk_add_f32 v[82:83], v[106:107], v[110:111]
	v_pk_add_f32 v[84:85], v[112:113], v[116:117]
	v_pk_add_f32 v[86:87], v[114:115], v[118:119]
	v_pk_add_f32 v[44:45], v[44:45], v[14:15]
	v_pk_add_f32 v[34:35], v[34:35], v[12:13]
	v_pk_add_f32 v[52:53], v[52:53], v[10:11]
	v_pk_add_f32 v[40:41], v[40:41], v[8:9]
	v_pk_add_f32 v[58:59], v[58:59], v[6:7]
	v_pk_add_f32 v[46:47], v[46:47], v[4:5]
	v_pk_add_f32 v[62:63], v[62:63], v[2:3]
	v_pk_add_f32 v[56:57], v[56:57], v[0:1]
	v_pk_add_f32 v[64:65], v[64:65], v[68:69]
	v_pk_add_f32 v[60:61], v[60:61], v[70:71]
	v_pk_add_f32 v[48:49], v[48:49], v[72:73]
	v_pk_add_f32 v[36:37], v[36:37], v[74:75]
	v_pk_add_f32 v[54:55], v[54:55], v[80:81]
	v_pk_add_f32 v[42:43], v[42:43], v[82:83]
	v_pk_add_f32 v[50:51], v[50:51], v[84:85]
	v_pk_add_f32 v[38:39], v[38:39], v[86:87]
	s_cbranch_vccz .LBB0_1418
	v_cvt_pk_bf16_f32 v0, v34, v35
	v_cvt_pk_bf16_f32 v1, v44, v45
	global_store_dwordx2 v[66:67], v[0:1], off
	v_cvt_pk_bf16_f32 v0, v40, v41
	v_cvt_pk_bf16_f32 v1, v52, v53
	global_store_dwordx2 v[66:67], v[0:1], off offset:512
	v_cvt_pk_bf16_f32 v0, v46, v47
	v_cvt_pk_bf16_f32 v1, v58, v59
	global_store_dwordx2 v[66:67], v[0:1], off offset:1024
	v_cvt_pk_bf16_f32 v0, v56, v57
	v_cvt_pk_bf16_f32 v1, v62, v63
	global_store_dwordx2 v[66:67], v[0:1], off offset:1536
	v_cvt_pk_bf16_f32 v0, v60, v61
	v_cvt_pk_bf16_f32 v1, v64, v65
	global_store_dwordx2 v[66:67], v[0:1], off offset:2048
	v_cvt_pk_bf16_f32 v0, v36, v37
	v_cvt_pk_bf16_f32 v1, v48, v49
	global_store_dwordx2 v[66:67], v[0:1], off offset:2560
	v_cvt_pk_bf16_f32 v0, v42, v43
	v_cvt_pk_bf16_f32 v1, v54, v55
	global_store_dwordx2 v[66:67], v[0:1], off offset:3072
	v_cvt_pk_bf16_f32 v0, v38, v39
	v_cvt_pk_bf16_f32 v1, v50, v51
	global_store_dwordx2 v[66:67], v[0:1], off offset:3584
.LBB0_1420:
	v_pk_mul_f32 v[10:11], v[34:35], v[34:35]
	v_pk_mul_f32 v[12:13], v[40:41], v[40:41]
	v_pk_mul_f32 v[4:5], v[44:45], v[44:45]
	v_pk_mul_f32 v[6:7], v[52:53], v[52:53]
	v_mov_b32_e32 v66, v10
	v_mov_b32_e32 v67, v12
	v_mov_b32_e32 v12, v11
	v_pk_mul_f32 v[0:1], v[58:59], v[58:59]
	v_pk_mul_f32 v[2:3], v[46:47], v[46:47]
	v_pk_add_f32 v[10:11], v[66:67], v[12:13]
	v_mov_b32_e32 v12, v4
	v_mov_b32_e32 v13, v6
	v_mov_b32_e32 v6, v5
	v_pk_add_f32 v[4:5], v[12:13], v[6:7]
	v_pk_mov_b32 v[6:7], v[2:3], v[0:1] op_sel:[1,0]
	v_mov_b32_e32 v3, v1
	v_pk_add_f32 v[0:1], v[6:7], v[2:3]
	v_pk_add_f32 v[4:5], v[10:11], v[4:5]
	v_pk_add_f32 v[0:1], v[0:1], v[0:1] op_sel_hi:[0,1]
	v_mul_f32_e32 v0, v56, v56
	v_pk_fma_f32 v[2:3], v[56:57], v[56:57], v[0:1] op_sel_hi:[1,1,0]
	v_mul_f32_e32 v0, v62, v62
	v_pk_add_f32 v[4:5], v[4:5], v[4:5] op_sel_hi:[0,1]
	v_pk_fma_f32 v[6:7], v[62:63], v[62:63], v[0:1] op_sel_hi:[1,1,0]
	v_mul_f32_e32 v2, v60, v60
	v_mul_f32_e32 v6, v61, v61
	v_mul_f32_e32 v0, v64, v64
	v_mul_f32_e32 v4, v65, v65
	v_pk_add_f32 v[2:3], v[2:3], v[6:7]
	v_pk_add_f32 v[0:1], v[0:1], v[4:5]
	global_load_dwordx4 v[4:7], v[22:23], off offset:1024 nt
	v_pk_add_f32 v[0:1], v[2:3], v[0:1]
	global_load_dwordx4 v[88:91], v[24:25], off nt
	global_load_dwordx4 v[92:95], v[26:27], off nt
	v_pk_add_f32 v[66:67], v[0:1], v[0:1] op_sel_hi:[0,1]
	global_load_dwordx4 v[0:3], v[22:23], off nt
	global_load_dwordx4 v[10:13], v[22:23], off offset:2048 nt
	global_load_dwordx4 v[84:87], v[22:23], off offset:3072 nt
	v_pk_mul_f32 v[8:9], v[48:49], v[48:49]
	v_pk_mul_f32 v[14:15], v[36:37], v[36:37]
	v_mul_f32_e32 v66, v51, v51
	v_pk_mov_b32 v[68:69], v[14:15], v[8:9] op_sel:[1,0]
	v_mov_b32_e32 v15, v9
	v_pk_add_f32 v[8:9], v[68:69], v[14:15]
	global_load_dwordx4 v[96:99], v[28:29], off nt
	global_load_dwordx4 v[100:103], v[30:31], off nt
	v_pk_add_f32 v[8:9], v[8:9], v[8:9] op_sel_hi:[0,1]
	v_mul_f32_e32 v8, v42, v42
	v_pk_fma_f32 v[14:15], v[42:43], v[42:43], v[8:9] op_sel_hi:[1,1,0]
	v_mul_f32_e32 v8, v54, v54
	v_pk_fma_f32 v[68:69], v[54:55], v[54:55], v[8:9] op_sel_hi:[1,1,0]
	v_mul_f32_e32 v14, v38, v38
	v_mul_f32_e32 v68, v39, v39
	v_mul_f32_e32 v8, v50, v50
	v_pk_add_f32 v[14:15], v[14:15], v[68:69]
	v_pk_add_f32 v[8:9], v[8:9], v[66:67]
	v_readlane_b32 s4, v250, 23
	v_pk_add_f32 v[8:9], v[14:15], v[8:9]
	v_readlane_b32 s12, v250, 31
	v_add_f32_e32 v8, v8, v9
	v_and_b32_e32 v9, 64, v78
	v_add_u32_e32 v14, 64, v9
	v_xor_b32_e32 v9, 1, v78
	v_cmp_lt_i32_e32 vcc, v9, v14
	v_readlane_b32 s13, v250, 32
	v_readlane_b32 s10, v250, 29
	v_cndmask_b32_e32 v9, v78, v9, vcc
	v_lshlrev_b32_e32 v9, 2, v9
	ds_bpermute_b32 v15, v9, v8
	v_readlane_b32 s11, v250, 30
	v_readlane_b32 s16, v250, 35
	v_readlane_b32 s17, v250, 36
	v_readlane_b32 s14, v250, 33
	s_waitcnt lgkmcnt(0)
	v_add_f32_e32 v8, v8, v15
	v_xor_b32_e32 v15, 2, v78
	v_cmp_lt_i32_e32 vcc, v15, v14
	v_readlane_b32 s15, v250, 34
	v_readlane_b32 s18, v250, 37
	v_cndmask_b32_e32 v15, v78, v15, vcc
	v_lshlrev_b32_e32 v32, 2, v15
	ds_bpermute_b32 v15, v32, v8
	v_readlane_b32 s19, v250, 38
	v_readlane_b32 s5, v250, 24
	v_readlane_b32 s6, v250, 25
	v_readlane_b32 s7, v250, 26
	s_waitcnt lgkmcnt(0)
	v_add_f32_e32 v8, v8, v15
	v_xor_b32_e32 v15, 4, v78
	v_cmp_lt_i32_e32 vcc, v15, v14
	v_readlane_b32 s8, v250, 27
	v_readlane_b32 s9, v250, 28
	v_cndmask_b32_e32 v15, v78, v15, vcc
	v_lshlrev_b32_e32 v80, 2, v15
	ds_bpermute_b32 v15, v80, v8
	s_waitcnt lgkmcnt(0)
	v_add_f32_e32 v8, v8, v15
	v_xor_b32_e32 v15, 8, v78
	v_cmp_lt_i32_e32 vcc, v15, v14
	s_waitcnt vmcnt(7)
	v_pk_mul_f32 v[70:71], v[40:41], v[4:5]
	v_cndmask_b32_e32 v15, v78, v15, vcc
	v_lshlrev_b32_e32 v81, 2, v15
	ds_bpermute_b32 v15, v81, v8
	v_pk_mul_f32 v[68:69], v[52:53], v[6:7]
	s_waitcnt vmcnt(4)
	v_pk_mul_f32 v[74:75], v[34:35], v[0:1]
	v_pk_mul_f32 v[72:73], v[44:45], v[2:3]
	v_pk_mul_f32 v[34:35], v[36:37], v[92:93]
	s_waitcnt lgkmcnt(0)
	v_add_f32_e32 v8, v8, v15
	v_xor_b32_e32 v15, 16, v78
	v_cmp_lt_i32_e32 vcc, v15, v14
	s_waitcnt vmcnt(3)
	v_pk_mul_f32 v[66:67], v[46:47], v[10:11]
	v_pk_mul_f32 v[58:59], v[58:59], v[12:13]
	v_cndmask_b32_e32 v15, v78, v15, vcc
	v_lshlrev_b32_e32 v82, 2, v15
	ds_bpermute_b32 v15, v82, v8
	s_waitcnt vmcnt(2)
	v_pk_mul_f32 v[52:53], v[56:57], v[84:85]
	v_pk_mul_f32 v[46:47], v[62:63], v[86:87]
	v_pk_mul_f32 v[44:45], v[60:61], v[88:89]
	v_pk_mul_f32 v[40:41], v[64:65], v[90:91]
	s_waitcnt lgkmcnt(0)
	v_add_f32_e32 v8, v8, v15
	v_xor_b32_e32 v15, 32, v78
	v_cmp_lt_i32_e32 vcc, v15, v14
	s_waitcnt vmcnt(1)
	v_pk_mul_f32 v[6:7], v[42:43], v[96:97]
	v_pk_mul_f32 v[4:5], v[54:55], v[98:99]
	v_cndmask_b32_e32 v14, v78, v15, vcc
	v_lshlrev_b32_e32 v83, 2, v14
	ds_bpermute_b32 v0, v83, v8
	v_pk_mul_f32 v[14:15], v[48:49], v[94:95]
	s_waitcnt vmcnt(0)
	v_pk_mul_f32 v[12:13], v[38:39], v[100:101]
	v_pk_mul_f32 v[10:11], v[50:51], v[102:103]
	s_waitcnt lgkmcnt(0)
	v_add_f32_e32 v0, v8, v0
	v_fmamk_f32 v0, v0, 0x3a000000, v17
	v_rsq_f32_e32 v8, v0
	v_lshl_add_u64 v[0:1], v[18:19], 1, s[40:41]
	v_mul_f32_e32 v2, v74, v8
	v_mul_f32_e32 v3, v75, v8
	v_cvt_pk_bf16_f32 v2, v2, v3
	v_mul_f32_e32 v3, v72, v8
	v_mul_f32_e32 v36, v73, v8
	v_cvt_pk_bf16_f32 v3, v3, v36
	global_store_dwordx2 v[0:1], v[2:3], off
	v_mul_f32_e32 v2, v70, v8
	v_mul_f32_e32 v3, v71, v8
	v_cvt_pk_bf16_f32 v2, v2, v3
	v_mul_f32_e32 v3, v68, v8
	v_mul_f32_e32 v36, v69, v8
	v_cvt_pk_bf16_f32 v3, v3, v36
	global_store_dwordx2 v[0:1], v[2:3], off offset:512
	v_mul_f32_e32 v2, v66, v8
	v_mul_f32_e32 v3, v67, v8
	v_cvt_pk_bf16_f32 v2, v2, v3
	v_mul_f32_e32 v3, v58, v8
	v_mul_f32_e32 v36, v59, v8
	v_cvt_pk_bf16_f32 v3, v3, v36
	global_store_dwordx2 v[0:1], v[2:3], off offset:1024
	v_mul_f32_e32 v2, v52, v8
	v_mul_f32_e32 v3, v53, v8
	v_cvt_pk_bf16_f32 v2, v2, v3
	v_mul_f32_e32 v3, v46, v8
	v_mul_f32_e32 v36, v47, v8
	v_cvt_pk_bf16_f32 v3, v3, v36
	global_store_dwordx2 v[0:1], v[2:3], off offset:1536
	v_mul_f32_e32 v2, v44, v8
	v_mul_f32_e32 v3, v45, v8
	v_cvt_pk_bf16_f32 v2, v2, v3
	v_mul_f32_e32 v3, v40, v8
	v_mul_f32_e32 v36, v41, v8
	v_cvt_pk_bf16_f32 v3, v3, v36
	global_store_dwordx2 v[0:1], v[2:3], off offset:2048
	v_mul_f32_e32 v2, v34, v8
	v_mul_f32_e32 v3, v35, v8
	v_cvt_pk_bf16_f32 v2, v2, v3
	v_mul_f32_e32 v3, v14, v8
	v_mul_f32_e32 v36, v15, v8
	v_cvt_pk_bf16_f32 v3, v3, v36
	global_store_dwordx2 v[0:1], v[2:3], off offset:2560
	v_mul_f32_e32 v2, v6, v8
	v_mul_f32_e32 v3, v7, v8
	v_cvt_pk_bf16_f32 v2, v2, v3
	v_mul_f32_e32 v3, v4, v8
	v_mul_f32_e32 v36, v5, v8
	v_cvt_pk_bf16_f32 v3, v3, v36
	global_store_dwordx2 v[0:1], v[2:3], off offset:3072
	v_mul_f32_e32 v2, v12, v8
	v_mul_f32_e32 v3, v13, v8
	v_cvt_pk_bf16_f32 v2, v2, v3
	v_mul_f32_e32 v3, v10, v8
	v_mul_f32_e32 v36, v11, v8
	v_cvt_pk_bf16_f32 v3, v3, v36
	global_store_dwordx2 v[0:1], v[2:3], off offset:3584
	v_mov_b32_e32 v0, v76
	s_nop 0
	v_lshl_add_u32 v0, v0, 3, 0
	v_add_u32_e32 v42, 0x20800, v0
	ds_read2st64_b64 v[0:3], v42 offset1:1
	ds_read2st64_b64 v[36:39], v42 offset0:2 offset1:3
	s_waitcnt lgkmcnt(1)
	v_fma_mix_f32 v43, v74, v0, 0 op_sel_hi:[0,1,0]
	v_fma_mix_f32 v0, v74, v0, 0 op_sel:[0,1,0] op_sel_hi:[0,1,0]
	v_fma_mix_f32 v48, v74, v1, 0 op_sel_hi:[0,1,0]
	v_fma_mix_f32 v1, v74, v1, 0 op_sel:[0,1,0] op_sel_hi:[0,1,0]
	v_fma_mix_f32 v43, v75, v2, v43 op_sel_hi:[0,1,0]
	v_fma_mix_f32 v0, v75, v2, v0 op_sel:[0,1,0] op_sel_hi:[0,1,0]
	v_fma_mix_f32 v2, v75, v3, v48 op_sel_hi:[0,1,0]
	v_fma_mix_f32 v1, v75, v3, v1 op_sel:[0,1,0] op_sel_hi:[0,1,0]
	s_waitcnt lgkmcnt(0)
	v_fma_mix_f32 v3, v72, v36, v43 op_sel_hi:[0,1,0]
	v_fma_mix_f32 v36, v72, v36, v0 op_sel:[0,1,0] op_sel_hi:[0,1,0]
	v_fma_mix_f32 v43, v72, v37, v2 op_sel_hi:[0,1,0]
	v_fma_mix_f32 v37, v72, v37, v1 op_sel:[0,1,0] op_sel_hi:[0,1,0]
	v_fma_mix_f32 v48, v73, v38, v3 op_sel_hi:[0,1,0]
	ds_read2st64_b64 v[0:3], v42 offset0:4 offset1:5
	v_fma_mix_f32 v49, v73, v38, v36 op_sel:[0,1,0] op_sel_hi:[0,1,0]
	v_fma_mix_f32 v43, v73, v39, v43 op_sel_hi:[0,1,0]
	v_fma_mix_f32 v50, v73, v39, v37 op_sel:[0,1,0] op_sel_hi:[0,1,0]
	ds_read2st64_b64 v[36:39], v42 offset0:6 offset1:7
	s_waitcnt lgkmcnt(1)
	v_fma_mix_f32 v48, v70, v0, v48 op_sel_hi:[0,1,0]
	v_fma_mix_f32 v0, v70, v0, v49 op_sel:[0,1,0] op_sel_hi:[0,1,0]
	v_fma_mix_f32 v43, v70, v1, v43 op_sel_hi:[0,1,0]
	v_fma_mix_f32 v1, v70, v1, v50 op_sel:[0,1,0] op_sel_hi:[0,1,0]
	v_fma_mix_f32 v48, v71, v2, v48 op_sel_hi:[0,1,0]
	v_fma_mix_f32 v0, v71, v2, v0 op_sel:[0,1,0] op_sel_hi:[0,1,0]
	v_fma_mix_f32 v2, v71, v3, v43 op_sel_hi:[0,1,0]
	v_fma_mix_f32 v1, v71, v3, v1 op_sel:[0,1,0] op_sel_hi:[0,1,0]
	s_waitcnt lgkmcnt(0)
	v_fma_mix_f32 v3, v68, v36, v48 op_sel_hi:[0,1,0]
	v_fma_mix_f32 v36, v68, v36, v0 op_sel:[0,1,0] op_sel_hi:[0,1,0]
	v_fma_mix_f32 v43, v68, v37, v2 op_sel_hi:[0,1,0]
	v_fma_mix_f32 v37, v68, v37, v1 op_sel:[0,1,0] op_sel_hi:[0,1,0]
	v_fma_mix_f32 v48, v69, v38, v3 op_sel_hi:[0,1,0]
	ds_read2st64_b64 v[0:3], v42 offset0:8 offset1:9
	v_fma_mix_f32 v49, v69, v38, v36 op_sel:[0,1,0] op_sel_hi:[0,1,0]
	v_fma_mix_f32 v43, v69, v39, v43 op_sel_hi:[0,1,0]
	v_fma_mix_f32 v50, v69, v39, v37 op_sel:[0,1,0] op_sel_hi:[0,1,0]
	ds_read2st64_b64 v[36:39], v42 offset0:10 offset1:11
	s_waitcnt lgkmcnt(1)
	v_fma_mix_f32 v48, v66, v0, v48 op_sel_hi:[0,1,0]
	v_fma_mix_f32 v0, v66, v0, v49 op_sel:[0,1,0] op_sel_hi:[0,1,0]
	v_fma_mix_f32 v43, v66, v1, v43 op_sel_hi:[0,1,0]
	v_fma_mix_f32 v1, v66, v1, v50 op_sel:[0,1,0] op_sel_hi:[0,1,0]
	v_fma_mix_f32 v48, v67, v2, v48 op_sel_hi:[0,1,0]
	v_fma_mix_f32 v0, v67, v2, v0 op_sel:[0,1,0] op_sel_hi:[0,1,0]
	v_fma_mix_f32 v2, v67, v3, v43 op_sel_hi:[0,1,0]
	v_fma_mix_f32 v1, v67, v3, v1 op_sel:[0,1,0] op_sel_hi:[0,1,0]
	s_waitcnt lgkmcnt(0)
	v_fma_mix_f32 v3, v58, v36, v48 op_sel_hi:[0,1,0]
	v_fma_mix_f32 v36, v58, v36, v0 op_sel:[0,1,0] op_sel_hi:[0,1,0]
	v_fma_mix_f32 v43, v58, v37, v2 op_sel_hi:[0,1,0]
	v_fma_mix_f32 v37, v58, v37, v1 op_sel:[0,1,0] op_sel_hi:[0,1,0]
	v_fma_mix_f32 v48, v59, v38, v3 op_sel_hi:[0,1,0]
	ds_read2st64_b64 v[0:3], v42 offset0:12 offset1:13
	v_fma_mix_f32 v49, v59, v38, v36 op_sel:[0,1,0] op_sel_hi:[0,1,0]
	v_fma_mix_f32 v43, v59, v39, v43 op_sel_hi:[0,1,0]
	v_fma_mix_f32 v50, v59, v39, v37 op_sel:[0,1,0] op_sel_hi:[0,1,0]
	ds_read2st64_b64 v[36:39], v42 offset0:14 offset1:15
	s_waitcnt lgkmcnt(1)
	v_fma_mix_f32 v48, v52, v0, v48 op_sel_hi:[0,1,0]
	v_fma_mix_f32 v0, v52, v0, v49 op_sel:[0,1,0] op_sel_hi:[0,1,0]
	v_fma_mix_f32 v43, v52, v1, v43 op_sel_hi:[0,1,0]
	v_fma_mix_f32 v1, v52, v1, v50 op_sel:[0,1,0] op_sel_hi:[0,1,0]
	v_fma_mix_f32 v48, v53, v2, v48 op_sel_hi:[0,1,0]
	v_fma_mix_f32 v0, v53, v2, v0 op_sel:[0,1,0] op_sel_hi:[0,1,0]
	v_fma_mix_f32 v2, v53, v3, v43 op_sel_hi:[0,1,0]
	v_fma_mix_f32 v1, v53, v3, v1 op_sel:[0,1,0] op_sel_hi:[0,1,0]
	s_waitcnt lgkmcnt(0)
	v_fma_mix_f32 v3, v46, v36, v48 op_sel_hi:[0,1,0]
	v_fma_mix_f32 v36, v46, v36, v0 op_sel:[0,1,0] op_sel_hi:[0,1,0]
	v_fma_mix_f32 v43, v46, v37, v2 op_sel_hi:[0,1,0]
	v_fma_mix_f32 v37, v46, v37, v1 op_sel:[0,1,0] op_sel_hi:[0,1,0]
	v_fma_mix_f32 v48, v47, v38, v3 op_sel_hi:[0,1,0]
	ds_read2st64_b64 v[0:3], v42 offset0:16 offset1:17
	v_fma_mix_f32 v49, v47, v38, v36 op_sel:[0,1,0] op_sel_hi:[0,1,0]
	v_fma_mix_f32 v43, v47, v39, v43 op_sel_hi:[0,1,0]
	v_fma_mix_f32 v50, v47, v39, v37 op_sel:[0,1,0] op_sel_hi:[0,1,0]
	ds_read2st64_b64 v[36:39], v42 offset0:18 offset1:19
	s_waitcnt lgkmcnt(1)
	v_fma_mix_f32 v48, v44, v0, v48 op_sel_hi:[0,1,0]
	v_fma_mix_f32 v0, v44, v0, v49 op_sel:[0,1,0] op_sel_hi:[0,1,0]
	v_fma_mix_f32 v43, v44, v1, v43 op_sel_hi:[0,1,0]
	v_fma_mix_f32 v1, v44, v1, v50 op_sel:[0,1,0] op_sel_hi:[0,1,0]
	v_fma_mix_f32 v48, v45, v2, v48 op_sel_hi:[0,1,0]
	v_fma_mix_f32 v0, v45, v2, v0 op_sel:[0,1,0] op_sel_hi:[0,1,0]
	v_fma_mix_f32 v2, v45, v3, v43 op_sel_hi:[0,1,0]
	v_fma_mix_f32 v1, v45, v3, v1 op_sel:[0,1,0] op_sel_hi:[0,1,0]
	s_waitcnt lgkmcnt(0)
	v_fma_mix_f32 v3, v40, v36, v48 op_sel_hi:[0,1,0]
	v_fma_mix_f32 v36, v40, v36, v0 op_sel:[0,1,0] op_sel_hi:[0,1,0]
	v_fma_mix_f32 v43, v40, v37, v2 op_sel_hi:[0,1,0]
	v_fma_mix_f32 v37, v40, v37, v1 op_sel:[0,1,0] op_sel_hi:[0,1,0]
	v_fma_mix_f32 v48, v41, v38, v3 op_sel_hi:[0,1,0]
	ds_read2st64_b64 v[0:3], v42 offset0:20 offset1:21
	v_fma_mix_f32 v49, v41, v38, v36 op_sel:[0,1,0] op_sel_hi:[0,1,0]
	v_fma_mix_f32 v43, v41, v39, v43 op_sel_hi:[0,1,0]
	v_fma_mix_f32 v50, v41, v39, v37 op_sel:[0,1,0] op_sel_hi:[0,1,0]
	ds_read2st64_b64 v[36:39], v42 offset0:22 offset1:23
	s_waitcnt lgkmcnt(1)
	v_fma_mix_f32 v48, v34, v0, v48 op_sel_hi:[0,1,0]
	v_fma_mix_f32 v0, v34, v0, v49 op_sel:[0,1,0] op_sel_hi:[0,1,0]
	v_fma_mix_f32 v43, v34, v1, v43 op_sel_hi:[0,1,0]
	v_fma_mix_f32 v1, v34, v1, v50 op_sel:[0,1,0] op_sel_hi:[0,1,0]
	v_fma_mix_f32 v48, v35, v2, v48 op_sel_hi:[0,1,0]
	v_fma_mix_f32 v0, v35, v2, v0 op_sel:[0,1,0] op_sel_hi:[0,1,0]
	v_fma_mix_f32 v2, v35, v3, v43 op_sel_hi:[0,1,0]
	v_fma_mix_f32 v1, v35, v3, v1 op_sel:[0,1,0] op_sel_hi:[0,1,0]
	s_waitcnt lgkmcnt(0)
	v_fma_mix_f32 v3, v14, v36, v48 op_sel_hi:[0,1,0]
	v_fma_mix_f32 v36, v14, v36, v0 op_sel:[0,1,0] op_sel_hi:[0,1,0]
	v_fma_mix_f32 v43, v14, v37, v2 op_sel_hi:[0,1,0]
	v_fma_mix_f32 v37, v14, v37, v1 op_sel:[0,1,0] op_sel_hi:[0,1,0]
	v_fma_mix_f32 v48, v15, v38, v3 op_sel_hi:[0,1,0]
	ds_read2st64_b64 v[0:3], v42 offset0:24 offset1:25
	v_fma_mix_f32 v49, v15, v38, v36 op_sel:[0,1,0] op_sel_hi:[0,1,0]
	v_fma_mix_f32 v43, v15, v39, v43 op_sel_hi:[0,1,0]
	v_fma_mix_f32 v50, v15, v39, v37 op_sel:[0,1,0] op_sel_hi:[0,1,0]
	ds_read2st64_b64 v[36:39], v42 offset0:26 offset1:27
	s_waitcnt lgkmcnt(1)
	v_fma_mix_f32 v48, v6, v0, v48 op_sel_hi:[0,1,0]
	v_fma_mix_f32 v0, v6, v0, v49 op_sel:[0,1,0] op_sel_hi:[0,1,0]
	v_fma_mix_f32 v43, v6, v1, v43 op_sel_hi:[0,1,0]
	v_fma_mix_f32 v1, v6, v1, v50 op_sel:[0,1,0] op_sel_hi:[0,1,0]
	v_fma_mix_f32 v48, v7, v2, v48 op_sel_hi:[0,1,0]
	v_fma_mix_f32 v49, v7, v2, v0 op_sel:[0,1,0] op_sel_hi:[0,1,0]
	v_fma_mix_f32 v43, v7, v3, v43 op_sel_hi:[0,1,0]
	v_fma_mix_f32 v50, v7, v3, v1 op_sel:[0,1,0] op_sel_hi:[0,1,0]
	global_load_dwordx4 v[0:3], v33, s[12:13] offset:16 nt
	s_waitcnt lgkmcnt(0)
	v_fma_mix_f32 v48, v4, v36, v48 op_sel_hi:[0,1,0]
	v_fma_mix_f32 v36, v4, v36, v49 op_sel:[0,1,0] op_sel_hi:[0,1,0]
	v_fma_mix_f32 v43, v4, v37, v43 op_sel_hi:[0,1,0]
	v_fma_mix_f32 v37, v4, v37, v50 op_sel:[0,1,0] op_sel_hi:[0,1,0]
	v_fma_mix_f32 v54, v5, v38, v48 op_sel_hi:[0,1,0]
	ds_read2st64_b64 v[48:51], v42 offset0:28 offset1:29
	v_fma_mix_f32 v55, v5, v38, v36 op_sel:[0,1,0] op_sel_hi:[0,1,0]
	v_fma_mix_f32 v43, v5, v39, v43 op_sel_hi:[0,1,0]
	v_fma_mix_f32 v56, v5, v39, v37 op_sel:[0,1,0] op_sel_hi:[0,1,0]
	ds_read2st64_b64 v[36:39], v42 offset0:30 offset1:31
	s_waitcnt lgkmcnt(1)
	v_fma_mix_f32 v42, v12, v48, v54 op_sel_hi:[0,1,0]
	v_fma_mix_f32 v48, v12, v48, v55 op_sel:[0,1,0] op_sel_hi:[0,1,0]
	v_fma_mix_f32 v43, v12, v49, v43 op_sel_hi:[0,1,0]
	v_fma_mix_f32 v54, v13, v50, v42 op_sel_hi:[0,1,0]
	v_fma_mix_f32 v48, v13, v50, v48 op_sel:[0,1,0] op_sel_hi:[0,1,0]
	v_fma_mix_f32 v50, v13, v51, v43 op_sel_hi:[0,1,0]
	s_waitcnt lgkmcnt(0)
	v_cvt_f32_f16_sdwa v43, v38 dst_sel:DWORD dst_unused:UNUSED_PAD src0_sel:WORD_1
	v_cvt_f32_f16_sdwa v42, v36 dst_sel:DWORD dst_unused:UNUSED_PAD src0_sel:WORD_1
	v_fma_mix_f32 v49, v12, v49, v56 op_sel:[0,1,0] op_sel_hi:[0,1,0]
	v_fma_mix_f32 v36, v10, v36, v54 op_sel_hi:[0,1,0]
	v_fma_mix_f32 v51, v13, v51, v49 op_sel:[0,1,0] op_sel_hi:[0,1,0]
	v_pk_mul_f32 v[42:43], v[10:11], v[42:43]
	v_fma_mix_f32 v54, v11, v38, v36 op_sel_hi:[0,1,0]
	v_add_f32_e32 v36, v42, v48
	v_cvt_f32_f16_e32 v49, v39
	v_cvt_f32_f16_e32 v48, v37
	v_cvt_f32_f16_sdwa v39, v39 dst_sel:DWORD dst_unused:UNUSED_PAD src0_sel:WORD_1
	v_cvt_f32_f16_sdwa v38, v37 dst_sel:DWORD dst_unused:UNUSED_PAD src0_sel:WORD_1
	v_add_f32_e32 v42, v43, v36
	v_pk_mul_f32 v[36:37], v[10:11], v[48:49]
	s_nop 0
	v_add_f32_e32 v36, v36, v50
	v_add_f32_e32 v43, v37, v36
	v_pk_mul_f32 v[36:37], v[10:11], v[38:39]
	v_cndmask_b32_e64 v39, v42, v54, s[2:3]
	v_add_f32_e32 v36, v36, v51
	v_add_f32_e32 v36, v37, v36
	v_cndmask_b32_e64 v37, v54, v42, s[2:3]
	v_cndmask_b32_e64 v38, v43, v36, s[2:3]
	ds_bpermute_b32 v37, v83, v37
	ds_bpermute_b32 v38, v83, v38
	v_cndmask_b32_e64 v36, v36, v43, s[2:3]
	s_waitcnt lgkmcnt(1)
	v_add_f32_e32 v37, v39, v37
	s_waitcnt lgkmcnt(0)
	v_add_f32_e32 v36, v36, v38
	v_cndmask_b32_e64 v38, v37, v36, s[68:69]
	ds_bpermute_b32 v38, v82, v38
	v_cndmask_b32_e64 v36, v36, v37, s[68:69]
	s_waitcnt lgkmcnt(0)
	v_add_f32_e32 v36, v36, v38
	ds_bpermute_b32 v37, v81, v36
	s_waitcnt lgkmcnt(0)
	v_add_f32_e32 v36, v36, v37
	ds_bpermute_b32 v37, v80, v36
	s_waitcnt lgkmcnt(0)
	v_add_f32_e32 v36, v36, v37
	ds_bpermute_b32 v37, v32, v36
	s_waitcnt lgkmcnt(0)
	v_add_f32_e32 v36, v36, v37
	ds_bpermute_b32 v37, v9, v36
	s_waitcnt lgkmcnt(0)
	v_add_f32_e32 v36, v36, v37
	s_nop 0
	v_readlane_b32 s10, v36, 0
	v_readlane_b32 s11, v36, 32
	v_readlane_b32 s12, v36, 16
	v_readlane_b32 s13, v36, 48
	s_waitcnt vmcnt(0)
	v_pk_fma_f32 v[36:37], v[8:9], s[10:11], v[0:1] op_sel_hi:[0,1,1]
	v_cmp_gt_f32_e32 vcc, v37, v36
	v_fma_f32 v0, s12, v8, v2
	v_fmac_f32_e32 v3, s13, v8
	v_cndmask_b32_e32 v1, v36, v37, vcc
	v_cmp_gt_f32_e64 s[10:11], v0, v1
	s_nop 1
	v_cndmask_b32_e64 v38, v1, v0, s[10:11]
	v_cndmask_b32_e64 v1, 0, 1, vcc
	v_cndmask_b32_e64 v1, v1, 2, s[10:11]
	v_cmp_gt_f32_e32 vcc, v3, v38
	s_nop 1
	v_cndmask_b32_e64 v1, v1, 3, vcc
	v_lshl_add_u32 v2, v1, 6, v76
	s_nop 0
	v_lshl_add_u32 v2, v2, 4, 0
	ds_read_b128 v[48:51], v2
	ds_read_b128 v[54:57], v2 offset:4096
	s_waitcnt lgkmcnt(1)
	v_fma_mix_f32 v39, v74, v48, 0 op_sel_hi:[0,1,0]
	v_fma_mix_f32 v42, v74, v48, 0 op_sel:[0,1,0] op_sel_hi:[0,1,0]
	v_fma_mix_f32 v43, v74, v49, 0 op_sel_hi:[0,1,0]
	v_fma_mix_f32 v48, v74, v49, 0 op_sel:[0,1,0] op_sel_hi:[0,1,0]
	v_fma_mix_f32 v49, v74, v50, 0 op_sel_hi:[0,1,0]
	v_fma_mix_f32 v60, v74, v50, 0 op_sel:[0,1,0] op_sel_hi:[0,1,0]
	v_fma_mix_f32 v61, v74, v51, 0 op_sel_hi:[0,1,0]
	v_fma_mix_f32 v62, v74, v51, 0 op_sel:[0,1,0] op_sel_hi:[0,1,0]
	s_waitcnt lgkmcnt(0)
	v_fma_mix_f32 v63, v75, v55, v48 op_sel:[0,1,0] op_sel_hi:[0,1,0]
	v_fma_mix_f32 v64, v75, v56, v49 op_sel_hi:[0,1,0]
	ds_read_b128 v[48:51], v2 offset:8192
	v_fma_mix_f32 v39, v75, v54, v39 op_sel_hi:[0,1,0]
	v_fma_mix_f32 v42, v75, v54, v42 op_sel:[0,1,0] op_sel_hi:[0,1,0]
	v_fma_mix_f32 v43, v75, v55, v43 op_sel_hi:[0,1,0]
	v_fma_mix_f32 v60, v75, v56, v60 op_sel:[0,1,0] op_sel_hi:[0,1,0]
	v_fma_mix_f32 v61, v75, v57, v61 op_sel_hi:[0,1,0]
	v_fma_mix_f32 v62, v75, v57, v62 op_sel:[0,1,0] op_sel_hi:[0,1,0]
	ds_read_b128 v[54:57], v2 offset:12288
	s_waitcnt lgkmcnt(1)
	v_fma_mix_f32 v39, v72, v48, v39 op_sel_hi:[0,1,0]
	v_fma_mix_f32 v42, v72, v48, v42 op_sel:[0,1,0] op_sel_hi:[0,1,0]
	v_fma_mix_f32 v43, v72, v49, v43 op_sel_hi:[0,1,0]
	v_fma_mix_f32 v48, v72, v49, v63 op_sel:[0,1,0] op_sel_hi:[0,1,0]
	v_fma_mix_f32 v49, v72, v50, v64 op_sel_hi:[0,1,0]
	v_fma_mix_f32 v60, v72, v50, v60 op_sel:[0,1,0] op_sel_hi:[0,1,0]
	v_fma_mix_f32 v61, v72, v51, v61 op_sel_hi:[0,1,0]
	v_fma_mix_f32 v62, v72, v51, v62 op_sel:[0,1,0] op_sel_hi:[0,1,0]
	s_waitcnt lgkmcnt(0)
	v_fma_mix_f32 v63, v73, v55, v48 op_sel:[0,1,0] op_sel_hi:[0,1,0]
	v_fma_mix_f32 v64, v73, v56, v49 op_sel_hi:[0,1,0]
	ds_read_b128 v[48:51], v2 offset:16384
	v_fma_mix_f32 v39, v73, v54, v39 op_sel_hi:[0,1,0]
	v_fma_mix_f32 v42, v73, v54, v42 op_sel:[0,1,0] op_sel_hi:[0,1,0]
	v_fma_mix_f32 v43, v73, v55, v43 op_sel_hi:[0,1,0]
	v_fma_mix_f32 v60, v73, v56, v60 op_sel:[0,1,0] op_sel_hi:[0,1,0]
	v_fma_mix_f32 v61, v73, v57, v61 op_sel_hi:[0,1,0]
	v_fma_mix_f32 v62, v73, v57, v62 op_sel:[0,1,0] op_sel_hi:[0,1,0]
	ds_read_b128 v[54:57], v2 offset:20480
	s_waitcnt lgkmcnt(1)
	v_fma_mix_f32 v39, v70, v48, v39 op_sel_hi:[0,1,0]
	v_fma_mix_f32 v42, v70, v48, v42 op_sel:[0,1,0] op_sel_hi:[0,1,0]
	v_fma_mix_f32 v43, v70, v49, v43 op_sel_hi:[0,1,0]
	v_fma_mix_f32 v48, v70, v49, v63 op_sel:[0,1,0] op_sel_hi:[0,1,0]
	v_fma_mix_f32 v49, v70, v50, v64 op_sel_hi:[0,1,0]
	v_fma_mix_f32 v60, v70, v50, v60 op_sel:[0,1,0] op_sel_hi:[0,1,0]
	v_fma_mix_f32 v61, v70, v51, v61 op_sel_hi:[0,1,0]
	v_fma_mix_f32 v62, v70, v51, v62 op_sel:[0,1,0] op_sel_hi:[0,1,0]
	s_waitcnt lgkmcnt(0)
	v_fma_mix_f32 v63, v71, v55, v48 op_sel:[0,1,0] op_sel_hi:[0,1,0]
	v_fma_mix_f32 v64, v71, v56, v49 op_sel_hi:[0,1,0]
	ds_read_b128 v[48:51], v2 offset:24576
	v_fma_mix_f32 v39, v71, v54, v39 op_sel_hi:[0,1,0]
	v_fma_mix_f32 v42, v71, v54, v42 op_sel:[0,1,0] op_sel_hi:[0,1,0]
	v_fma_mix_f32 v43, v71, v55, v43 op_sel_hi:[0,1,0]
	v_fma_mix_f32 v60, v71, v56, v60 op_sel:[0,1,0] op_sel_hi:[0,1,0]
	v_fma_mix_f32 v61, v71, v57, v61 op_sel_hi:[0,1,0]
	v_fma_mix_f32 v62, v71, v57, v62 op_sel:[0,1,0] op_sel_hi:[0,1,0]
	ds_read_b128 v[54:57], v2 offset:28672
	s_waitcnt lgkmcnt(1)
	v_fma_mix_f32 v39, v68, v48, v39 op_sel_hi:[0,1,0]
	v_fma_mix_f32 v42, v68, v48, v42 op_sel:[0,1,0] op_sel_hi:[0,1,0]
	v_fma_mix_f32 v43, v68, v49, v43 op_sel_hi:[0,1,0]
	v_fma_mix_f32 v48, v68, v49, v63 op_sel:[0,1,0] op_sel_hi:[0,1,0]
	v_fma_mix_f32 v49, v68, v50, v64 op_sel_hi:[0,1,0]
	v_fma_mix_f32 v60, v68, v50, v60 op_sel:[0,1,0] op_sel_hi:[0,1,0]
	v_fma_mix_f32 v61, v68, v51, v61 op_sel_hi:[0,1,0]
	v_fma_mix_f32 v62, v68, v51, v62 op_sel:[0,1,0] op_sel_hi:[0,1,0]
	s_waitcnt lgkmcnt(0)
	v_fma_mix_f32 v63, v69, v55, v48 op_sel:[0,1,0] op_sel_hi:[0,1,0]
	v_fma_mix_f32 v64, v69, v56, v49 op_sel_hi:[0,1,0]
	ds_read_b128 v[48:51], v2 offset:32768
	v_fma_mix_f32 v39, v69, v54, v39 op_sel_hi:[0,1,0]
	v_fma_mix_f32 v42, v69, v54, v42 op_sel:[0,1,0] op_sel_hi:[0,1,0]
	v_fma_mix_f32 v43, v69, v55, v43 op_sel_hi:[0,1,0]
	v_fma_mix_f32 v60, v69, v56, v60 op_sel:[0,1,0] op_sel_hi:[0,1,0]
	v_fma_mix_f32 v61, v69, v57, v61 op_sel_hi:[0,1,0]
	v_fma_mix_f32 v62, v69, v57, v62 op_sel:[0,1,0] op_sel_hi:[0,1,0]
	ds_read_b128 v[54:57], v2 offset:36864
	s_waitcnt lgkmcnt(1)
	v_fma_mix_f32 v39, v66, v48, v39 op_sel_hi:[0,1,0]
	v_fma_mix_f32 v42, v66, v48, v42 op_sel:[0,1,0] op_sel_hi:[0,1,0]
	v_fma_mix_f32 v43, v66, v49, v43 op_sel_hi:[0,1,0]
	v_fma_mix_f32 v48, v66, v49, v63 op_sel:[0,1,0] op_sel_hi:[0,1,0]
	v_fma_mix_f32 v49, v66, v50, v64 op_sel_hi:[0,1,0]
	v_fma_mix_f32 v60, v66, v50, v60 op_sel:[0,1,0] op_sel_hi:[0,1,0]
	v_fma_mix_f32 v61, v66, v51, v61 op_sel_hi:[0,1,0]
	v_fma_mix_f32 v62, v66, v51, v62 op_sel:[0,1,0] op_sel_hi:[0,1,0]
	s_waitcnt lgkmcnt(0)
	v_fma_mix_f32 v63, v67, v55, v48 op_sel:[0,1,0] op_sel_hi:[0,1,0]
	v_fma_mix_f32 v64, v67, v56, v49 op_sel_hi:[0,1,0]
	ds_read_b128 v[48:51], v2 offset:40960
	v_fma_mix_f32 v39, v67, v54, v39 op_sel_hi:[0,1,0]
	v_fma_mix_f32 v42, v67, v54, v42 op_sel:[0,1,0] op_sel_hi:[0,1,0]
	v_fma_mix_f32 v43, v67, v55, v43 op_sel_hi:[0,1,0]
	v_fma_mix_f32 v60, v67, v56, v60 op_sel:[0,1,0] op_sel_hi:[0,1,0]
	v_fma_mix_f32 v61, v67, v57, v61 op_sel_hi:[0,1,0]
	v_fma_mix_f32 v62, v67, v57, v62 op_sel:[0,1,0] op_sel_hi:[0,1,0]
	ds_read_b128 v[54:57], v2 offset:45056
	s_waitcnt lgkmcnt(1)
	v_fma_mix_f32 v39, v58, v48, v39 op_sel_hi:[0,1,0]
	v_fma_mix_f32 v42, v58, v48, v42 op_sel:[0,1,0] op_sel_hi:[0,1,0]
	v_fma_mix_f32 v43, v58, v49, v43 op_sel_hi:[0,1,0]
	v_fma_mix_f32 v48, v58, v49, v63 op_sel:[0,1,0] op_sel_hi:[0,1,0]
	v_fma_mix_f32 v49, v58, v50, v64 op_sel_hi:[0,1,0]
	v_fma_mix_f32 v60, v58, v50, v60 op_sel:[0,1,0] op_sel_hi:[0,1,0]
	v_fma_mix_f32 v61, v58, v51, v61 op_sel_hi:[0,1,0]
	v_fma_mix_f32 v58, v58, v51, v62 op_sel:[0,1,0] op_sel_hi:[0,1,0]
	s_waitcnt lgkmcnt(0)
	v_fma_mix_f32 v62, v59, v55, v48 op_sel:[0,1,0] op_sel_hi:[0,1,0]
	v_fma_mix_f32 v63, v59, v56, v49 op_sel_hi:[0,1,0]
	ds_read_b128 v[48:51], v2 offset:49152
	v_fma_mix_f32 v39, v59, v54, v39 op_sel_hi:[0,1,0]
	v_fma_mix_f32 v42, v59, v54, v42 op_sel:[0,1,0] op_sel_hi:[0,1,0]
	v_fma_mix_f32 v43, v59, v55, v43 op_sel_hi:[0,1,0]
	v_fma_mix_f32 v60, v59, v56, v60 op_sel:[0,1,0] op_sel_hi:[0,1,0]
	v_fma_mix_f32 v61, v59, v57, v61 op_sel_hi:[0,1,0]
	v_fma_mix_f32 v58, v59, v57, v58 op_sel:[0,1,0] op_sel_hi:[0,1,0]
	ds_read_b128 v[54:57], v2 offset:53248
	s_waitcnt lgkmcnt(1)
	v_fma_mix_f32 v39, v52, v48, v39 op_sel_hi:[0,1,0]
	v_fma_mix_f32 v42, v52, v48, v42 op_sel:[0,1,0] op_sel_hi:[0,1,0]
	v_fma_mix_f32 v43, v52, v49, v43 op_sel_hi:[0,1,0]
	v_fma_mix_f32 v48, v52, v49, v62 op_sel:[0,1,0] op_sel_hi:[0,1,0]
	v_fma_mix_f32 v49, v52, v50, v63 op_sel_hi:[0,1,0]
	v_fma_mix_f32 v59, v52, v50, v60 op_sel:[0,1,0] op_sel_hi:[0,1,0]
	v_fma_mix_f32 v60, v52, v51, v61 op_sel_hi:[0,1,0]
	v_fma_mix_f32 v52, v52, v51, v58 op_sel:[0,1,0] op_sel_hi:[0,1,0]
	s_waitcnt lgkmcnt(0)
	v_fma_mix_f32 v58, v53, v55, v48 op_sel:[0,1,0] op_sel_hi:[0,1,0]
	v_fma_mix_f32 v61, v53, v56, v49 op_sel_hi:[0,1,0]
	ds_read_b128 v[48:51], v2 offset:57344
	v_fma_mix_f32 v39, v53, v54, v39 op_sel_hi:[0,1,0]
	v_fma_mix_f32 v42, v53, v54, v42 op_sel:[0,1,0] op_sel_hi:[0,1,0]
	v_fma_mix_f32 v43, v53, v55, v43 op_sel_hi:[0,1,0]
	v_fma_mix_f32 v56, v53, v56, v59 op_sel:[0,1,0] op_sel_hi:[0,1,0]
	v_fma_mix_f32 v59, v53, v57, v60 op_sel_hi:[0,1,0]
	v_fma_mix_f32 v57, v53, v57, v52 op_sel:[0,1,0] op_sel_hi:[0,1,0]
	ds_read_b128 v[52:55], v2 offset:61440
	s_waitcnt lgkmcnt(1)
	v_fma_mix_f32 v39, v46, v48, v39 op_sel_hi:[0,1,0]
	v_fma_mix_f32 v42, v46, v48, v42 op_sel:[0,1,0] op_sel_hi:[0,1,0]
	v_fma_mix_f32 v48, v46, v49, v58 op_sel:[0,1,0] op_sel_hi:[0,1,0]
	v_fma_mix_f32 v43, v46, v49, v43 op_sel_hi:[0,1,0]
	v_fma_mix_f32 v49, v46, v50, v61 op_sel_hi:[0,1,0]
	v_fma_mix_f32 v50, v46, v50, v56 op_sel:[0,1,0] op_sel_hi:[0,1,0]
	v_fma_mix_f32 v56, v46, v51, v59 op_sel_hi:[0,1,0]
	v_fma_mix_f32 v46, v46, v51, v57 op_sel:[0,1,0] op_sel_hi:[0,1,0]
	s_waitcnt lgkmcnt(0)
	v_fma_mix_f32 v57, v47, v53, v48 op_sel:[0,1,0] op_sel_hi:[0,1,0]
	v_add_u32_e32 v48, 0x10000, v2
	v_fma_mix_f32 v39, v47, v52, v39 op_sel_hi:[0,1,0]
	v_fma_mix_f32 v42, v47, v52, v42 op_sel:[0,1,0] op_sel_hi:[0,1,0]
	v_fma_mix_f32 v43, v47, v53, v43 op_sel_hi:[0,1,0]
	v_fma_mix_f32 v58, v47, v54, v49 op_sel_hi:[0,1,0]
	v_fma_mix_f32 v59, v47, v54, v50 op_sel:[0,1,0] op_sel_hi:[0,1,0]
	ds_read_b128 v[48:51], v48
	v_fma_mix_f32 v56, v47, v55, v56 op_sel_hi:[0,1,0]
	v_fma_mix_f32 v46, v47, v55, v46 op_sel:[0,1,0] op_sel_hi:[0,1,0]
	v_add_u32_e32 v47, 0x11000, v2
	ds_read_b128 v[52:55], v47
	s_waitcnt lgkmcnt(1)
	v_fma_mix_f32 v42, v44, v48, v42 op_sel:[0,1,0] op_sel_hi:[0,1,0]
	v_fma_mix_f32 v39, v44, v48, v39 op_sel_hi:[0,1,0]
	v_fma_mix_f32 v43, v44, v49, v43 op_sel_hi:[0,1,0]
	v_fma_mix_f32 v47, v44, v49, v57 op_sel:[0,1,0] op_sel_hi:[0,1,0]
	v_fma_mix_f32 v48, v44, v50, v58 op_sel_hi:[0,1,0]
	v_fma_mix_f32 v49, v44, v50, v59 op_sel:[0,1,0] op_sel_hi:[0,1,0]
	v_fma_mix_f32 v50, v44, v51, v56 op_sel_hi:[0,1,0]
	v_fma_mix_f32 v44, v44, v51, v46 op_sel:[0,1,0] op_sel_hi:[0,1,0]
	s_waitcnt lgkmcnt(0)
	v_fma_mix_f32 v51, v45, v52, v42 op_sel:[0,1,0] op_sel_hi:[0,1,0]
	v_add_u32_e32 v42, 0x12000, v2
	v_fma_mix_f32 v39, v45, v52, v39 op_sel_hi:[0,1,0]
	v_fma_mix_f32 v52, v45, v53, v43 op_sel_hi:[0,1,0]
	v_fma_mix_f32 v53, v45, v53, v47 op_sel:[0,1,0] op_sel_hi:[0,1,0]
	v_fma_mix_f32 v56, v45, v54, v48 op_sel_hi:[0,1,0]
	v_fma_mix_f32 v54, v45, v54, v49 op_sel:[0,1,0] op_sel_hi:[0,1,0]
	ds_read_b128 v[46:49], v42
	v_add_u32_e32 v42, 0x13000, v2
	v_fma_mix_f32 v50, v45, v55, v50 op_sel_hi:[0,1,0]
	v_fma_mix_f32 v55, v45, v55, v44 op_sel:[0,1,0] op_sel_hi:[0,1,0]
	ds_read_b128 v[42:45], v42
	s_waitcnt lgkmcnt(1)
	v_fma_mix_f32 v39, v40, v46, v39 op_sel_hi:[0,1,0]
	v_fma_mix_f32 v46, v40, v46, v51 op_sel:[0,1,0] op_sel_hi:[0,1,0]
	v_fma_mix_f32 v51, v40, v47, v52 op_sel_hi:[0,1,0]
	v_fma_mix_f32 v47, v40, v47, v53 op_sel:[0,1,0] op_sel_hi:[0,1,0]
	v_fma_mix_f32 v52, v40, v48, v56 op_sel_hi:[0,1,0]
	v_fma_mix_f32 v48, v40, v48, v54 op_sel:[0,1,0] op_sel_hi:[0,1,0]
	v_fma_mix_f32 v50, v40, v49, v50 op_sel_hi:[0,1,0]
	v_fma_mix_f32 v40, v40, v49, v55 op_sel:[0,1,0] op_sel_hi:[0,1,0]
	s_waitcnt lgkmcnt(0)
	v_fma_mix_f32 v39, v41, v42, v39 op_sel_hi:[0,1,0]
	v_fma_mix_f32 v53, v41, v42, v46 op_sel:[0,1,0] op_sel_hi:[0,1,0]
	v_add_u32_e32 v42, 0x14000, v2
	v_fma_mix_f32 v54, v41, v43, v47 op_sel:[0,1,0] op_sel_hi:[0,1,0]
	v_fma_mix_f32 v52, v41, v44, v52 op_sel_hi:[0,1,0]
	v_fma_mix_f32 v44, v41, v44, v48 op_sel:[0,1,0] op_sel_hi:[0,1,0]
	ds_read_b128 v[46:49], v42
	v_fma_mix_f32 v50, v41, v45, v50 op_sel_hi:[0,1,0]
	v_fma_mix_f32 v45, v41, v45, v40 op_sel:[0,1,0] op_sel_hi:[0,1,0]
	v_add_u32_e32 v40, 0x15000, v2
	v_fma_mix_f32 v51, v41, v43, v51 op_sel_hi:[0,1,0]
	ds_read_b128 v[40:43], v40
	s_waitcnt lgkmcnt(1)
	v_fma_mix_f32 v39, v34, v46, v39 op_sel_hi:[0,1,0]
	v_fma_mix_f32 v46, v34, v46, v53 op_sel:[0,1,0] op_sel_hi:[0,1,0]
	v_fma_mix_f32 v51, v34, v47, v51 op_sel_hi:[0,1,0]
	v_fma_mix_f32 v47, v34, v47, v54 op_sel:[0,1,0] op_sel_hi:[0,1,0]
	v_fma_mix_f32 v52, v34, v48, v52 op_sel_hi:[0,1,0]
	v_fma_mix_f32 v44, v34, v48, v44 op_sel:[0,1,0] op_sel_hi:[0,1,0]
	v_fma_mix_f32 v48, v34, v49, v50 op_sel_hi:[0,1,0]
	v_fma_mix_f32 v34, v34, v49, v45 op_sel:[0,1,0] op_sel_hi:[0,1,0]
	s_waitcnt lgkmcnt(0)
	v_fma_mix_f32 v39, v35, v40, v39 op_sel_hi:[0,1,0]
	v_fma_mix_f32 v49, v35, v40, v46 op_sel:[0,1,0] op_sel_hi:[0,1,0]
	v_add_u32_e32 v40, 0x16000, v2
	v_fma_mix_f32 v50, v35, v41, v51 op_sel_hi:[0,1,0]
	v_fma_mix_f32 v51, v35, v41, v47 op_sel:[0,1,0] op_sel_hi:[0,1,0]
	v_fma_mix_f32 v52, v35, v42, v52 op_sel_hi:[0,1,0]
	v_fma_mix_f32 v53, v35, v42, v44 op_sel:[0,1,0] op_sel_hi:[0,1,0]
	ds_read_b128 v[44:47], v40
	v_fma_mix_f32 v48, v35, v43, v48 op_sel_hi:[0,1,0]
	v_fma_mix_f32 v34, v35, v43, v34 op_sel:[0,1,0] op_sel_hi:[0,1,0]
	v_add_u32_e32 v35, 0x17000, v2
	ds_read_b128 v[40:43], v35
	s_waitcnt lgkmcnt(1)
	v_fma_mix_f32 v35, v14, v44, v39 op_sel_hi:[0,1,0]
	v_fma_mix_f32 v39, v14, v44, v49 op_sel:[0,1,0] op_sel_hi:[0,1,0]
	v_fma_mix_f32 v44, v14, v45, v50 op_sel_hi:[0,1,0]
	v_fma_mix_f32 v45, v14, v45, v51 op_sel:[0,1,0] op_sel_hi:[0,1,0]
	v_fma_mix_f32 v49, v14, v46, v52 op_sel_hi:[0,1,0]
	v_fma_mix_f32 v46, v14, v46, v53 op_sel:[0,1,0] op_sel_hi:[0,1,0]
	v_fma_mix_f32 v48, v14, v47, v48 op_sel_hi:[0,1,0]
	v_fma_mix_f32 v14, v14, v47, v34 op_sel:[0,1,0] op_sel_hi:[0,1,0]
	s_waitcnt lgkmcnt(0)
	v_fma_mix_f32 v34, v15, v40, v35 op_sel_hi:[0,1,0]
	v_fma_mix_f32 v35, v15, v40, v39 op_sel:[0,1,0] op_sel_hi:[0,1,0]
	v_add_u32_e32 v40, 0x18000, v2
	v_fma_mix_f32 v39, v15, v41, v44 op_sel_hi:[0,1,0]
	v_fma_mix_f32 v50, v15, v41, v45 op_sel:[0,1,0] op_sel_hi:[0,1,0]
	v_fma_mix_f32 v49, v15, v42, v49 op_sel_hi:[0,1,0]
	v_fma_mix_f32 v51, v15, v42, v46 op_sel:[0,1,0] op_sel_hi:[0,1,0]
	ds_read_b128 v[44:47], v40
	v_fma_mix_f32 v48, v15, v43, v48 op_sel_hi:[0,1,0]
	v_fma_mix_f32 v14, v15, v43, v14 op_sel:[0,1,0] op_sel_hi:[0,1,0]
	v_add_u32_e32 v15, 0x19000, v2
	ds_read_b128 v[40:43], v15
	s_waitcnt lgkmcnt(1)
	v_fma_mix_f32 v15, v6, v44, v34 op_sel_hi:[0,1,0]
	v_fma_mix_f32 v34, v6, v44, v35 op_sel:[0,1,0] op_sel_hi:[0,1,0]
	v_fma_mix_f32 v35, v6, v45, v39 op_sel_hi:[0,1,0]
	v_fma_mix_f32 v39, v6, v45, v50 op_sel:[0,1,0] op_sel_hi:[0,1,0]
	v_fma_mix_f32 v44, v6, v46, v49 op_sel_hi:[0,1,0]
	v_fma_mix_f32 v45, v6, v46, v51 op_sel:[0,1,0] op_sel_hi:[0,1,0]
	v_fma_mix_f32 v48, v6, v47, v48 op_sel_hi:[0,1,0]
	v_fma_mix_f32 v6, v6, v47, v14 op_sel:[0,1,0] op_sel_hi:[0,1,0]
	s_waitcnt lgkmcnt(0)
	v_fma_mix_f32 v14, v7, v40, v15 op_sel_hi:[0,1,0]
	v_fma_mix_f32 v15, v7, v40, v34 op_sel:[0,1,0] op_sel_hi:[0,1,0]
	v_add_u32_e32 v40, 0x1a000, v2
	v_fma_mix_f32 v34, v7, v41, v35 op_sel_hi:[0,1,0]
	v_fma_mix_f32 v35, v7, v41, v39 op_sel:[0,1,0] op_sel_hi:[0,1,0]
	v_fma_mix_f32 v39, v7, v42, v44 op_sel_hi:[0,1,0]
	v_fma_mix_f32 v49, v7, v42, v45 op_sel:[0,1,0] op_sel_hi:[0,1,0]
	ds_read_b128 v[44:47], v40
	v_fma_mix_f32 v48, v7, v43, v48 op_sel_hi:[0,1,0]
	v_fma_mix_f32 v6, v7, v43, v6 op_sel:[0,1,0] op_sel_hi:[0,1,0]
	v_add_u32_e32 v7, 0x1b000, v2
	ds_read_b128 v[40:43], v7
	s_waitcnt lgkmcnt(1)
	v_fma_mix_f32 v7, v4, v44, v14 op_sel_hi:[0,1,0]
	v_fma_mix_f32 v14, v4, v44, v15 op_sel:[0,1,0] op_sel_hi:[0,1,0]
	v_fma_mix_f32 v15, v4, v45, v34 op_sel_hi:[0,1,0]
	v_fma_mix_f32 v34, v4, v45, v35 op_sel:[0,1,0] op_sel_hi:[0,1,0]
	v_fma_mix_f32 v35, v4, v46, v39 op_sel_hi:[0,1,0]
	v_fma_mix_f32 v39, v4, v46, v49 op_sel:[0,1,0] op_sel_hi:[0,1,0]
	v_fma_mix_f32 v48, v4, v47, v48 op_sel_hi:[0,1,0]
	v_fma_mix_f32 v4, v4, v47, v6 op_sel:[0,1,0] op_sel_hi:[0,1,0]
	s_waitcnt lgkmcnt(0)
	v_fma_mix_f32 v6, v5, v40, v7 op_sel_hi:[0,1,0]
	v_fma_mix_f32 v7, v5, v40, v14 op_sel:[0,1,0] op_sel_hi:[0,1,0]
	v_fma_mix_f32 v14, v5, v41, v15 op_sel_hi:[0,1,0]
	v_fma_mix_f32 v15, v5, v41, v34 op_sel:[0,1,0] op_sel_hi:[0,1,0]
	v_fma_mix_f32 v34, v5, v42, v35 op_sel_hi:[0,1,0]
	v_fma_mix_f32 v35, v5, v42, v39 op_sel:[0,1,0] op_sel_hi:[0,1,0]
	v_add_u32_e32 v39, 0x1c000, v2
	ds_read_b128 v[44:47], v39
	v_fma_mix_f32 v39, v5, v43, v48 op_sel_hi:[0,1,0]
	v_fma_mix_f32 v4, v5, v43, v4 op_sel:[0,1,0] op_sel_hi:[0,1,0]
	v_add_u32_e32 v5, 0x1d000, v2
	ds_read_b128 v[40:43], v5
	s_waitcnt lgkmcnt(1)
	v_fma_mix_f32 v5, v12, v44, v6 op_sel_hi:[0,1,0]
	v_fma_mix_f32 v6, v12, v44, v7 op_sel:[0,1,0] op_sel_hi:[0,1,0]
	v_fma_mix_f32 v7, v12, v45, v14 op_sel_hi:[0,1,0]
	v_fma_mix_f32 v14, v12, v45, v15 op_sel:[0,1,0] op_sel_hi:[0,1,0]
	v_fma_mix_f32 v15, v12, v46, v34 op_sel_hi:[0,1,0]
	s_waitcnt lgkmcnt(0)
	v_fma_mix_f32 v53, v13, v42, v15 op_sel_hi:[0,1,0]
	v_lshlrev_b32_e32 v15, 5, v1
	v_fma_mix_f32 v34, v12, v46, v35 op_sel:[0,1,0] op_sel_hi:[0,1,0]
	v_fma_mix_f32 v35, v12, v47, v39 op_sel_hi:[0,1,0]
	v_fma_mix_f32 v12, v12, v47, v4 op_sel:[0,1,0] op_sel_hi:[0,1,0]
	v_fma_mix_f32 v39, v13, v40, v5 op_sel_hi:[0,1,0]
	v_fma_mix_f32 v40, v13, v40, v6 op_sel:[0,1,0] op_sel_hi:[0,1,0]
	v_fma_mix_f32 v52, v13, v41, v7 op_sel_hi:[0,1,0]
	global_load_dwordx4 v[4:7], v15, s[16:17] offset:144 nt
	global_load_dwordx4 v[44:47], v15, s[16:17] offset:128 nt
	v_fma_mix_f32 v41, v13, v41, v14 op_sel:[0,1,0] op_sel_hi:[0,1,0]
	v_add_u32_e32 v14, 0x1e000, v2
	ds_read_b128 v[48:51], v14
	v_add_u32_e32 v2, 0x1f000, v2
	v_fma_mix_f32 v34, v13, v42, v34 op_sel:[0,1,0] op_sel_hi:[0,1,0]
	v_fma_mix_f32 v35, v13, v43, v35 op_sel_hi:[0,1,0]
	v_fma_mix_f32 v42, v13, v43, v12 op_sel:[0,1,0] op_sel_hi:[0,1,0]
	ds_read_b128 v[12:15], v2
	s_waitcnt lgkmcnt(1)
	v_fma_mix_f32 v2, v10, v48, v39 op_sel_hi:[0,1,0]
	v_fma_mix_f32 v39, v10, v48, v40 op_sel:[0,1,0] op_sel_hi:[0,1,0]
	v_fma_mix_f32 v40, v10, v49, v52 op_sel_hi:[0,1,0]
	v_fma_mix_f32 v41, v10, v49, v41 op_sel:[0,1,0] op_sel_hi:[0,1,0]
	v_fma_mix_f32 v43, v10, v50, v53 op_sel_hi:[0,1,0]
	v_fma_mix_f32 v34, v10, v50, v34 op_sel:[0,1,0] op_sel_hi:[0,1,0]
	v_fma_mix_f32 v35, v10, v51, v35 op_sel_hi:[0,1,0]
	v_fma_mix_f32 v10, v10, v51, v42 op_sel:[0,1,0] op_sel_hi:[0,1,0]
	s_waitcnt lgkmcnt(0)
	v_fma_mix_f32 v2, v11, v12, v2 op_sel_hi:[0,1,0]
	v_fma_mix_f32 v12, v11, v12, v39 op_sel:[0,1,0] op_sel_hi:[0,1,0]
	v_fma_mix_f32 v39, v11, v13, v40 op_sel_hi:[0,1,0]
	v_fma_mix_f32 v13, v11, v13, v41 op_sel:[0,1,0] op_sel_hi:[0,1,0]
	v_fma_mix_f32 v40, v11, v14, v43 op_sel_hi:[0,1,0]
	v_fma_mix_f32 v14, v11, v14, v34 op_sel:[0,1,0] op_sel_hi:[0,1,0]
	v_fma_mix_f32 v34, v11, v15, v35 op_sel_hi:[0,1,0]
	v_fma_mix_f32 v10, v11, v15, v10 op_sel:[0,1,0] op_sel_hi:[0,1,0]
	v_cndmask_b32_e64 v11, v39, v13, s[2:3]
	v_cndmask_b32_e64 v41, v2, v12, s[2:3]
	v_cndmask_b32_e64 v2, v12, v2, s[2:3]
	v_cndmask_b32_e64 v12, v13, v39, s[2:3]
	ds_bpermute_b32 v11, v83, v11
	v_cndmask_b32_e64 v13, v40, v14, s[2:3]
	v_cndmask_b32_e64 v15, v34, v10, s[2:3]
	ds_bpermute_b32 v41, v83, v41
	ds_bpermute_b32 v13, v83, v13
	ds_bpermute_b32 v15, v83, v15
	s_waitcnt lgkmcnt(3)
	v_add_f32_e32 v11, v12, v11
	v_cndmask_b32_e64 v12, v14, v40, s[2:3]
	v_cndmask_b32_e64 v10, v10, v34, s[2:3]
	s_waitcnt lgkmcnt(2)
	v_add_f32_e32 v2, v2, v41
	s_waitcnt lgkmcnt(1)
	v_add_f32_e32 v12, v12, v13
	s_waitcnt lgkmcnt(0)
	v_add_f32_e32 v10, v10, v15
	v_cndmask_b32_e64 v13, v2, v11, s[68:69]
	v_cndmask_b32_e64 v14, v12, v10, s[68:69]
	ds_bpermute_b32 v13, v82, v13
	ds_bpermute_b32 v14, v82, v14
	v_cndmask_b32_e64 v2, v11, v2, s[68:69]
	v_cndmask_b32_e64 v10, v10, v12, s[68:69]
	s_waitcnt lgkmcnt(1)
	v_add_f32_e32 v2, v2, v13
	s_waitcnt lgkmcnt(0)
	v_add_f32_e32 v10, v10, v14
	v_cndmask_b32_e64 v11, v2, v10, s[70:71]
	ds_bpermute_b32 v11, v81, v11
	v_cndmask_b32_e64 v2, v10, v2, s[70:71]
	s_waitcnt lgkmcnt(0)
	v_add_f32_e32 v2, v2, v11
	ds_bpermute_b32 v10, v80, v2
	s_waitcnt lgkmcnt(0)
	v_add_f32_e32 v2, v2, v10
	ds_bpermute_b32 v10, v32, v2
	s_waitcnt lgkmcnt(0)
	v_add_f32_e32 v2, v2, v10
	ds_bpermute_b32 v9, v9, v2
	s_waitcnt lgkmcnt(0)
	v_add_f32_e32 v2, v2, v9
	s_nop 0
	v_readlane_b32 s10, v2, 0
	v_readlane_b32 s11, v2, 32
	v_readlane_b32 s12, v2, 16
	v_readlane_b32 s13, v2, 48
	v_readlane_b32 s14, v2, 8
	s_waitcnt vmcnt(0)
	v_pk_fma_f32 v[10:11], v[8:9], s[10:11], v[44:45] op_sel_hi:[0,1,1]
	v_cmp_gt_f32_e64 s[10:11], v11, v10
	v_readlane_b32 s15, v2, 40
	v_readlane_b32 s16, v2, 24
	v_readlane_b32 s17, v2, 56
	v_fma_f32 v9, s12, v8, v46
	v_cndmask_b32_e64 v2, v10, v11, s[10:11]
	v_fma_f32 v12, s15, v8, v5
	v_cndmask_b32_e64 v5, 0, 1, s[10:11]
	v_cmp_gt_f32_e64 s[10:11], v9, v2
	v_fmac_f32_e32 v47, s13, v8
	v_fma_f32 v4, s14, v8, v4
	v_cndmask_b32_e64 v2, v2, v9, s[10:11]
	v_cndmask_b32_e64 v5, v5, 2, s[10:11]
	v_cmp_gt_f32_e64 s[10:11], v47, v2
	v_fma_f32 v6, s16, v8, v6
	v_fmac_f32_e32 v7, s17, v8
	v_cndmask_b32_e64 v2, v2, v47, s[10:11]
	v_cndmask_b32_e64 v5, v5, 3, s[10:11]
	v_cmp_gt_f32_e64 s[10:11], v4, v2
	v_cmp_nlt_f32_e64 s[18:19], s53, v10
	s_nop 0
	v_cndmask_b32_e64 v2, v2, v4, s[10:11]
	v_cndmask_b32_e64 v5, v5, 4, s[10:11]
	v_cmp_gt_f32_e64 s[10:11], v12, v2
	s_nop 1
	v_cndmask_b32_e64 v2, v2, v12, s[10:11]
	v_cndmask_b32_e64 v8, v5, 5, s[10:11]
	v_cmp_ngt_f32_e64 s[10:11], v6, v2
	s_nop 1
	v_cndmask_b32_e64 v5, v6, v2, s[10:11]
	v_cndmask_b32_e64 v2, 6, v8, s[10:11]
	v_cmp_gt_f32_e64 s[14:15], v7, v5
	v_cmp_ngt_f32_e64 s[12:13], v7, v5
	s_nop 0
	v_cndmask_b32_e64 v2, v2, 7, s[14:15]
	v_cmp_eq_u32_e64 s[16:17], 0, v2
	s_or_b64 s[16:17], s[16:17], s[18:19]
	s_or_b64 s[14:15], s[10:11], s[14:15]
	v_cndmask_b32_e64 v8, v10, v79, s[16:17]
	v_cndmask_b32_e64 v10, 0, -1, s[16:17]
	v_cmp_ne_u32_e64 s[16:17], 1, v2
	v_cmp_gt_f32_e64 s[18:19], v11, v8
	s_and_b64 s[16:17], s[16:17], s[18:19]
	v_cndmask_b32_e64 v8, v8, v11, s[16:17]
	v_cndmask_b32_e64 v10, v10, 1, s[16:17]
	v_cmp_ne_u32_e64 s[16:17], 2, v2
	v_cmp_gt_f32_e64 s[18:19], v9, v8
	s_and_b64 s[16:17], s[16:17], s[18:19]
	v_cndmask_b32_e64 v8, v8, v9, s[16:17]
	v_cndmask_b32_e64 v9, v10, 2, s[16:17]
	v_cmp_ne_u32_e64 s[16:17], 3, v2
	v_cmp_gt_f32_e64 s[18:19], v47, v8
	s_and_b64 s[16:17], s[16:17], s[18:19]
	v_cndmask_b32_e64 v8, v8, v47, s[16:17]
	v_cndmask_b32_e64 v9, v9, 3, s[16:17]
	v_cmp_ne_u32_e64 s[16:17], 4, v2
	v_cmp_gt_f32_e64 s[18:19], v4, v8
	s_and_b64 s[16:17], s[16:17], s[18:19]
	v_cndmask_b32_e64 v4, v8, v4, s[16:17]
	v_cndmask_b32_e64 v8, v9, 4, s[16:17]
	v_cmp_ne_u32_e64 s[16:17], 5, v2
	v_cmp_gt_f32_e64 s[18:19], v12, v4
	s_and_b64 s[16:17], s[16:17], s[18:19]
	v_cndmask_b32_e64 v4, v4, v12, s[16:17]
	v_cmp_gt_f32_e64 s[10:11], v6, v4
	v_cndmask_b32_e64 v8, v8, 5, s[16:17]
	s_and_b64 s[10:11], s[14:15], s[10:11]
	v_cndmask_b32_e64 v4, v4, v6, s[10:11]
	v_cndmask_b32_e64 v6, v8, 6, s[10:11]
	s_and_saveexec_b64 s[14:15], s[12:13]
	s_cbranch_execz .LBB0_1424
	v_cmp_gt_f32_e64 s[10:11], v7, v4
	s_and_saveexec_b64 s[12:13], s[10:11]
	v_mov_b32_e32 v6, 7
	v_mov_b32_e32 v4, v7
	s_or_b64 exec, exec, s[12:13]
	v_mov_b32_e32 v7, v5
